# topk: pack tag constants rematerialized at use (frees 99 VGPRs); all 8 key-row load groups of a half issued up front with counted vmcnt waits
# speedup vs baseline: 1.0047x; 1.0047x over previous
.LBB0_695:
	v_readlane_b32 s6, v255, 7
	v_readlane_b32 s7, v255, 8
	s_lshl_b64 s[6:7], s[6:7], 19
	v_readlane_b32 s8, v253, 25
	v_mov_b32_e32 v0, v175
	s_waitcnt vmcnt(0)
	s_waitcnt lgkmcnt(0)
	s_barrier
	s_add_u32 s6, s8, s6
	v_readlane_b32 s8, v253, 26
	s_addc_u32 s7, s8, s7
	v_and_b32_e32 v1, 63, v0
	v_bfe_u32 v2, v0, 5, 1
	v_ashrrev_i32_e32 v3, 6, v0
	v_and_b32_e32 v206, 31, v0
	v_lshlrev_b32_e32 v4, 13, v3
	v_lshlrev_b32_e32 v0, 3, v2
	v_lshlrev_b32_e32 v144, 4, v2
	v_lshlrev_b32_e32 v5, 2, v1
	v_lshlrev_b32_e32 v66, 2, v2
	v_lshl_add_u64 v[64:65], s[6:7], 0, v[144:145]
	v_add3_u32 v207, 0, v4, v5
	v_cmp_gt_u32_e64 s[38:39], 32, v1
	v_lshlrev_b32_e32 v144, 1, v0
	v_lshl_or_b32 v208, v3, 5, v206
	s_mov_b32 s18, 0
	s_branch .LBB0_698

.LBB0_704:
	v_cndmask_b32_e64 v0, 0, 1, s[6:7]
	s_lshl_b32 s36, s8, 8
	v_cmp_ne_u32_e32 vcc, 1, v0
	v_lshl_add_u64 v[0:1], v[178:179], 0, s[36:37]
	global_load_dwordx4 v[44:47], v[0:1], off
	global_load_dwordx4 v[40:43], v[0:1], off offset:32
	global_load_dwordx4 v[36:39], v[0:1], off offset:64
	global_load_dwordx4 v[32:35], v[0:1], off offset:96
	global_load_dwordx4 v[28:31], v[0:1], off offset:128
	global_load_dwordx4 v[24:27], v[0:1], off offset:160
	global_load_dwordx4 v[20:23], v[0:1], off offset:192
	global_load_dwordx4 v[16:19], v[0:1], off offset:224
	v_lshl_or_b32 v180, s8, 7, v209
	v_ashrrev_i32_e32 v181, 31, v180
	v_lshlrev_b64 v[0:1], 8, v[180:181]
	v_lshl_add_u64 v[60:61], v[64:65], 0, v[0:1]
	global_load_dwordx4 v[0:3], v[60:61], off
	global_load_dwordx4 v[48:51], v[60:61], off offset:32
	global_load_dwordx4 v[52:55], v[60:61], off offset:64
	global_load_dwordx4 v[56:59], v[60:61], off offset:96
	global_load_dwordx4 v[68:71], v[60:61], off offset:128
	global_load_dwordx4 v[72:75], v[60:61], off offset:160
	global_load_dwordx4 v[76:79], v[60:61], off offset:192
	global_load_dwordx4 v[80:83], v[60:61], off offset:224
	s_mov_b32 s12, 0x2000
	s_mov_b32 s13, 0
	v_lshl_add_u64 v[186:187], v[60:61], 0, s[12:13]
	global_load_dwordx4 v[84:87], v[186:187], off
	global_load_dwordx4 v[88:91], v[186:187], off offset:32
	global_load_dwordx4 v[92:95], v[186:187], off offset:64
	global_load_dwordx4 v[96:99], v[186:187], off offset:96
	global_load_dwordx4 v[100:103], v[186:187], off offset:128
	global_load_dwordx4 v[104:107], v[186:187], off offset:160
	global_load_dwordx4 v[108:111], v[186:187], off offset:192
	global_load_dwordx4 v[112:115], v[186:187], off offset:224
	v_lshl_add_u64 v[188:189], v[186:187], 0, s[12:13]
	global_load_dwordx4 v[116:119], v[188:189], off
	global_load_dwordx4 v[120:123], v[188:189], off offset:32
	global_load_dwordx4 v[124:127], v[188:189], off offset:64
	global_load_dwordx4 v[128:131], v[188:189], off offset:96
	global_load_dwordx4 v[132:135], v[188:189], off offset:128
	global_load_dwordx4 v[136:139], v[188:189], off offset:160
	global_load_dwordx4 v[140:143], v[188:189], off offset:192
	global_load_dwordx4 v[152:155], v[188:189], off offset:224
	v_lshl_add_u64 v[186:187], v[188:189], 0, s[12:13]
	global_load_dwordx4 v[156:159], v[186:187], off
	global_load_dwordx4 v[160:163], v[186:187], off offset:32
	global_load_dwordx4 v[164:167], v[186:187], off offset:64
	global_load_dwordx4 v[168:171], v[186:187], off offset:96
	s_nop 15
	s_nop 15
	s_waitcnt vmcnt(24)
	v_mfma_f32_32x32x16_bf16 v[0:15], v[0:3], v[44:47], 0
	v_mfma_f32_32x32x16_bf16 v[0:15], v[48:51], v[40:43], v[0:15]
	v_mfma_f32_32x32x16_bf16 v[0:15], v[52:55], v[36:39], v[0:15]
	v_mfma_f32_32x32x16_bf16 v[0:15], v[56:59], v[32:35], v[0:15]
	s_nop 15
	s_nop 15
	global_load_dwordx4 v[48:51], v[186:187], off offset:128
	global_load_dwordx4 v[52:55], v[186:187], off offset:160
	global_load_dwordx4 v[56:59], v[186:187], off offset:192
	global_load_dwordx4 v[60:63], v[186:187], off offset:224
	s_nop 15
	s_nop 15
	s_waitcnt vmcnt(27)
	v_mfma_f32_32x32x16_bf16 v[0:15], v[68:71], v[28:31], v[0:15]
	s_waitcnt vmcnt(26)
	v_mfma_f32_32x32x16_bf16 v[0:15], v[72:75], v[24:27], v[0:15]
	s_waitcnt vmcnt(25)
	v_mfma_f32_32x32x16_bf16 v[0:15], v[76:79], v[20:23], v[0:15]
	s_waitcnt vmcnt(24)
	v_mfma_f32_32x32x16_bf16 v[0:15], v[80:83], v[16:19], v[0:15]
	s_nop 15
	s_nop 15
	v_or_b32_e32 v172, 1, v66
	v_xor_b32_e32 v174, 0x7e, v66
	s_nop 9
	v_cmp_gt_i32_e64 s[6:7], 0, v1
	v_xor_b32_e32 v67, 0x7f, v66
	v_and_b32_e32 v1, 0xffffff80, v1
	v_cndmask_b32_e64 v172, v174, v172, s[6:7]
	v_cmp_gt_i32_e64 s[6:7], 0, v0
	v_and_b32_e32 v0, 0xffffff80, v0
	v_or_b32_e32 v210, v172, v1
	v_cndmask_b32_e64 v67, v67, v66, s[6:7]
	v_or_b32_e32 v211, v67, v0
	v_or_b32_e32 v1, 3, v66
	v_xor_b32_e32 v173, 0x7c, v66
	v_cmp_gt_i32_e64 s[6:7], 0, v3
	v_or_b32_e32 v0, 2, v66
	v_xor_b32_e32 v190, 0x7d, v66
	v_cndmask_b32_e64 v1, v173, v1, s[6:7]
	v_cmp_gt_i32_e64 s[6:7], 0, v2
	v_and_b32_e32 v3, 0xffffff80, v3
	v_and_b32_e32 v2, 0xffffff80, v2
	v_cndmask_b32_e64 v0, v190, v0, s[6:7]
	v_or_b32_e32 v173, v1, v3
	v_or_b32_e32 v1, 9, v66
	v_xor_b32_e32 v3, 0x76, v66
	v_cmp_gt_i32_e64 s[6:7], 0, v5
	v_or_b32_e32 v212, v0, v2
	v_or_b32_e32 v0, 8, v66
	v_cndmask_b32_e64 v1, v3, v1, s[6:7]
	v_xor_b32_e32 v2, 0x77, v66
	v_cmp_gt_i32_e64 s[6:7], 0, v4
	v_and_b32_e32 v3, 0xffffff80, v4
	s_nop 0
	v_cndmask_b32_e64 v0, v2, v0, s[6:7]
	v_and_b32_e32 v2, 0xffffff80, v5
	v_or_b32_e32 v213, v1, v2
	v_or_b32_e32 v214, v0, v3
	v_or_b32_e32 v1, 11, v66
	v_xor_b32_e32 v3, 0x74, v66
	v_cmp_gt_i32_e64 s[6:7], 0, v7
	v_or_b32_e32 v0, 10, v66
	v_xor_b32_e32 v2, 0x75, v66
	v_cndmask_b32_e64 v1, v3, v1, s[6:7]
	v_cmp_gt_i32_e64 s[6:7], 0, v6
	v_and_b32_e32 v3, 0xffffff80, v6
	s_nop 0
	v_cndmask_b32_e64 v0, v2, v0, s[6:7]
	v_and_b32_e32 v2, 0xffffff80, v7
	v_or_b32_e32 v215, v1, v2
	v_or_b32_e32 v216, v0, v3
	v_or_b32_e32 v1, 17, v66
	v_xor_b32_e32 v3, 0x6e, v66
	v_cmp_gt_i32_e64 s[6:7], 0, v9
	v_or_b32_e32 v0, 16, v66
	v_xor_b32_e32 v2, 0x6f, v66
	v_cndmask_b32_e64 v1, v3, v1, s[6:7]
	v_cmp_gt_i32_e64 s[6:7], 0, v8
	v_and_b32_e32 v3, 0xffffff80, v8
	s_nop 0
	v_cndmask_b32_e64 v0, v2, v0, s[6:7]
	v_and_b32_e32 v2, 0xffffff80, v9
	v_or_b32_e32 v217, v1, v2
	v_or_b32_e32 v218, v0, v3
	v_or_b32_e32 v1, 19, v66
	v_xor_b32_e32 v3, 0x6c, v66
	v_cmp_gt_i32_e64 s[6:7], 0, v11
	v_or_b32_e32 v0, 18, v66
	v_xor_b32_e32 v2, 0x6d, v66
	v_cndmask_b32_e64 v1, v3, v1, s[6:7]
	v_cmp_gt_i32_e64 s[6:7], 0, v10
	v_and_b32_e32 v3, 0xffffff80, v10
	s_nop 0
	v_cndmask_b32_e64 v0, v2, v0, s[6:7]
	v_and_b32_e32 v2, 0xffffff80, v11
	v_or_b32_e32 v219, v1, v2
	v_or_b32_e32 v220, v0, v3
	v_or_b32_e32 v1, 25, v66
	v_xor_b32_e32 v3, 0x66, v66
	v_cmp_gt_i32_e64 s[6:7], 0, v13
	v_or_b32_e32 v0, 24, v66
	v_xor_b32_e32 v2, 0x67, v66
	v_cndmask_b32_e64 v1, v3, v1, s[6:7]
	v_cmp_gt_i32_e64 s[6:7], 0, v12
	v_and_b32_e32 v3, 0xffffff80, v12
	s_nop 0
	v_cndmask_b32_e64 v0, v2, v0, s[6:7]
	v_and_b32_e32 v2, 0xffffff80, v13
	v_or_b32_e32 v221, v1, v2
	v_or_b32_e32 v1, 27, v66
	v_cmp_gt_i32_e64 s[6:7], 0, v15
	v_or_b32_e32 v222, v0, v3
	v_and_b32_e32 v2, 0xffffff80, v15
	v_xor_b32_e32 v0, 0x64, v66
	v_cndmask_b32_e64 v0, v0, v1, s[6:7]
	v_cmp_gt_i32_e64 s[6:7], 0, v14
	v_and_b32_e32 v3, 0xffffff80, v14
	v_or_b32_e32 v223, v0, v2
	v_xor_b32_e32 v1, 0x65, v66
	v_or_b32_e32 v188, 26, v66
	v_cndmask_b32_e64 v1, v1, v188, s[6:7]
	v_or_b32_e32 v224, v1, v3
	s_nop 15
	s_nop 15
	s_waitcnt vmcnt(23)
	v_mfma_f32_32x32x16_bf16 v[0:15], v[84:87], v[44:47], 0
	s_waitcnt vmcnt(22)
	v_mfma_f32_32x32x16_bf16 v[0:15], v[88:91], v[40:43], v[0:15]
	s_waitcnt vmcnt(21)
	v_mfma_f32_32x32x16_bf16 v[0:15], v[92:95], v[36:39], v[0:15]
	s_waitcnt vmcnt(20)
	v_mfma_f32_32x32x16_bf16 v[0:15], v[96:99], v[32:35], v[0:15]
	s_nop 15
	s_nop 15
	s_nop 15
	s_nop 15
	s_waitcnt vmcnt(19)
	v_mfma_f32_32x32x16_bf16 v[0:15], v[100:103], v[28:31], v[0:15]
	s_waitcnt vmcnt(18)
	v_mfma_f32_32x32x16_bf16 v[0:15], v[104:107], v[24:27], v[0:15]
	s_waitcnt vmcnt(17)
	v_mfma_f32_32x32x16_bf16 v[0:15], v[108:111], v[20:23], v[0:15]
	s_waitcnt vmcnt(16)
	v_mfma_f32_32x32x16_bf16 v[0:15], v[112:115], v[16:19], v[0:15]
	s_nop 15
	s_nop 15
	s_nop 3
	v_cmp_gt_i32_e64 s[6:7], 0, v1
	v_and_b32_e32 v1, 0xffffff80, v1
	s_nop 0
	v_xor_b32_e32 v181, 0x5e, v66
	v_or_b32_e32 v188, 33, v66
	v_cndmask_b32_e64 v181, v181, v188, s[6:7]
	v_cmp_gt_i32_e64 s[6:7], 0, v0
	v_and_b32_e32 v0, 0xffffff80, v0
	v_or_b32_e32 v225, v181, v1
	v_xor_b32_e32 v190, 0x5f, v66
	v_or_b32_e32 v188, 32, v66
	v_cndmask_b32_e64 v190, v190, v188, s[6:7]
	v_cmp_gt_i32_e64 s[6:7], 0, v3
	v_or_b32_e32 v226, v190, v0
	v_and_b32_e32 v3, 0xffffff80, v3
	v_xor_b32_e32 v0, 0x5c, v66
	v_or_b32_e32 v188, 35, v66
	v_cndmask_b32_e64 v0, v0, v188, s[6:7]
	v_cmp_gt_i32_e64 s[6:7], 0, v2
	v_and_b32_e32 v2, 0xffffff80, v2
	v_or_b32_e32 v227, v0, v3
	v_xor_b32_e32 v1, 0x5d, v66
	v_or_b32_e32 v188, 34, v66
	v_cndmask_b32_e64 v1, v1, v188, s[6:7]
	v_cmp_gt_i32_e64 s[6:7], 0, v5
	v_or_b32_e32 v228, v1, v2
	v_and_b32_e32 v2, 0xffffff80, v5
	v_xor_b32_e32 v0, 0x56, v66
	v_or_b32_e32 v188, 41, v66
	v_cndmask_b32_e64 v0, v0, v188, s[6:7]
	v_cmp_gt_i32_e64 s[6:7], 0, v4
	v_and_b32_e32 v3, 0xffffff80, v4
	v_or_b32_e32 v229, v0, v2
	v_xor_b32_e32 v1, 0x57, v66
	v_or_b32_e32 v188, 40, v66
	v_cndmask_b32_e64 v1, v1, v188, s[6:7]
	v_cmp_gt_i32_e64 s[6:7], 0, v7
	v_or_b32_e32 v230, v1, v3
	v_and_b32_e32 v2, 0xffffff80, v7
	v_xor_b32_e32 v0, 0x54, v66
	v_or_b32_e32 v188, 43, v66
	v_cndmask_b32_e64 v0, v0, v188, s[6:7]
	v_cmp_gt_i32_e64 s[6:7], 0, v6
	v_and_b32_e32 v3, 0xffffff80, v6
	v_or_b32_e32 v231, v0, v2
	v_xor_b32_e32 v1, 0x55, v66
	v_or_b32_e32 v188, 42, v66
	v_cndmask_b32_e64 v1, v1, v188, s[6:7]
	v_cmp_gt_i32_e64 s[6:7], 0, v9
	v_or_b32_e32 v232, v1, v3
	v_and_b32_e32 v2, 0xffffff80, v9
	v_xor_b32_e32 v0, 0x4e, v66
	v_or_b32_e32 v188, 49, v66
	v_cndmask_b32_e64 v0, v0, v188, s[6:7]
	v_cmp_gt_i32_e64 s[6:7], 0, v8
	v_and_b32_e32 v3, 0xffffff80, v8
	v_or_b32_e32 v233, v0, v2
	v_xor_b32_e32 v1, 0x4f, v66
	v_or_b32_e32 v188, 48, v66
	v_cndmask_b32_e64 v1, v1, v188, s[6:7]
	v_cmp_gt_i32_e64 s[6:7], 0, v11
	v_or_b32_e32 v234, v1, v3
	v_and_b32_e32 v2, 0xffffff80, v11
	v_xor_b32_e32 v0, 0x4c, v66
	v_or_b32_e32 v188, 51, v66
	v_cndmask_b32_e64 v0, v0, v188, s[6:7]
	v_cmp_gt_i32_e64 s[6:7], 0, v10
	v_and_b32_e32 v3, 0xffffff80, v10
	v_or_b32_e32 v235, v0, v2
	v_xor_b32_e32 v1, 0x4d, v66
	v_or_b32_e32 v188, 50, v66
	v_cndmask_b32_e64 v1, v1, v188, s[6:7]
	v_cmp_gt_i32_e64 s[6:7], 0, v13
	v_or_b32_e32 v236, v1, v3
	v_and_b32_e32 v2, 0xffffff80, v13
	v_xor_b32_e32 v0, 0x46, v66
	v_or_b32_e32 v188, 57, v66
	v_cndmask_b32_e64 v0, v0, v188, s[6:7]
	v_cmp_gt_i32_e64 s[6:7], 0, v12
	v_and_b32_e32 v3, 0xffffff80, v12
	v_or_b32_e32 v237, v0, v2
	v_xor_b32_e32 v1, 0x47, v66
	v_or_b32_e32 v188, 56, v66
	v_cndmask_b32_e64 v1, v1, v188, s[6:7]
	v_cmp_gt_i32_e64 s[6:7], 0, v15
	v_or_b32_e32 v238, v1, v3
	v_and_b32_e32 v2, 0xffffff80, v15
	v_xor_b32_e32 v0, 0x44, v66
	v_or_b32_e32 v188, 59, v66
	v_cndmask_b32_e64 v0, v0, v188, s[6:7]
	v_cmp_gt_i32_e64 s[6:7], 0, v14
	v_and_b32_e32 v3, 0xffffff80, v14
	v_or_b32_e32 v239, v0, v2
	v_xor_b32_e32 v1, 0x45, v66
	v_or_b32_e32 v188, 58, v66
	v_cndmask_b32_e64 v1, v1, v188, s[6:7]
	v_or_b32_e32 v240, v1, v3
	s_nop 15
	s_nop 15
	s_waitcnt vmcnt(15)
	v_mfma_f32_32x32x16_bf16 v[0:15], v[116:119], v[44:47], 0
	s_waitcnt vmcnt(14)
	v_mfma_f32_32x32x16_bf16 v[0:15], v[120:123], v[40:43], v[0:15]
	s_waitcnt vmcnt(13)
	v_mfma_f32_32x32x16_bf16 v[0:15], v[124:127], v[36:39], v[0:15]
	s_waitcnt vmcnt(12)
	v_mfma_f32_32x32x16_bf16 v[0:15], v[128:131], v[32:35], v[0:15]
	s_nop 15
	s_nop 15
	s_nop 15
	s_nop 15
	s_waitcnt vmcnt(11)
	v_mfma_f32_32x32x16_bf16 v[0:15], v[132:135], v[28:31], v[0:15]
	s_waitcnt vmcnt(10)
	v_mfma_f32_32x32x16_bf16 v[0:15], v[136:139], v[24:27], v[0:15]
	s_waitcnt vmcnt(9)
	v_mfma_f32_32x32x16_bf16 v[0:15], v[140:143], v[20:23], v[0:15]
	s_waitcnt vmcnt(8)
	v_mfma_f32_32x32x16_bf16 v[0:15], v[152:155], v[16:19], v[0:15]
	s_nop 15
	s_nop 15
	s_nop 3
	v_cmp_gt_i32_e64 s[6:7], 0, v1
	v_and_b32_e32 v1, 0xffffff80, v1
	s_nop 0
	v_xor_b32_e32 v182, 62, v66
	v_or_b32_e32 v188, 0x41, v66
	v_cndmask_b32_e64 v182, v182, v188, s[6:7]
	v_cmp_gt_i32_e64 s[6:7], 0, v0
	v_and_b32_e32 v0, 0xffffff80, v0
	v_or_b32_e32 v182, v182, v1
	v_xor_b32_e32 v183, 63, v66
	v_or_b32_e32 v188, 64, v66
	v_cndmask_b32_e64 v183, v183, v188, s[6:7]
	v_cmp_gt_i32_e64 s[6:7], 0, v3
	v_or_b32_e32 v183, v183, v0
	v_and_b32_e32 v3, 0xffffff80, v3
	v_xor_b32_e32 v0, 60, v66
	v_or_b32_e32 v188, 0x43, v66
	v_cndmask_b32_e64 v0, v0, v188, s[6:7]
	v_cmp_gt_i32_e64 s[6:7], 0, v2
	v_and_b32_e32 v2, 0xffffff80, v2
	v_or_b32_e32 v241, v0, v3
	v_xor_b32_e32 v1, 61, v66
	v_or_b32_e32 v188, 0x42, v66
	v_cndmask_b32_e64 v1, v1, v188, s[6:7]
	v_cmp_gt_i32_e64 s[6:7], 0, v5
	v_or_b32_e32 v242, v1, v2
	v_and_b32_e32 v2, 0xffffff80, v5
	v_xor_b32_e32 v0, 54, v66
	v_or_b32_e32 v188, 0x49, v66
	v_cndmask_b32_e64 v0, v0, v188, s[6:7]
	v_cmp_gt_i32_e64 s[6:7], 0, v4
	v_and_b32_e32 v3, 0xffffff80, v4
	v_or_b32_e32 v243, v0, v2
	v_xor_b32_e32 v1, 55, v66
	v_or_b32_e32 v188, 0x48, v66
	v_cndmask_b32_e64 v1, v1, v188, s[6:7]
	v_cmp_gt_i32_e64 s[6:7], 0, v7
	v_or_b32_e32 v244, v1, v3
	v_and_b32_e32 v2, 0xffffff80, v7
	v_xor_b32_e32 v0, 52, v66
	v_or_b32_e32 v188, 0x4b, v66
	v_cndmask_b32_e64 v0, v0, v188, s[6:7]
	v_cmp_gt_i32_e64 s[6:7], 0, v6
	v_and_b32_e32 v3, 0xffffff80, v6
	v_or_b32_e32 v245, v0, v2
	v_xor_b32_e32 v1, 53, v66
	v_or_b32_e32 v188, 0x4a, v66
	v_cndmask_b32_e64 v1, v1, v188, s[6:7]
	v_cmp_gt_i32_e64 s[6:7], 0, v9
	v_or_b32_e32 v246, v1, v3
	v_and_b32_e32 v2, 0xffffff80, v9
	v_xor_b32_e32 v0, 46, v66
	v_or_b32_e32 v188, 0x51, v66
	v_cndmask_b32_e64 v0, v0, v188, s[6:7]
	v_cmp_gt_i32_e64 s[6:7], 0, v8
	v_and_b32_e32 v3, 0xffffff80, v8
	v_or_b32_e32 v247, v0, v2
	v_xor_b32_e32 v1, 47, v66
	v_or_b32_e32 v188, 0x50, v66
	v_cndmask_b32_e64 v1, v1, v188, s[6:7]
	v_cmp_gt_i32_e64 s[6:7], 0, v11
	v_or_b32_e32 v248, v1, v3
	v_and_b32_e32 v2, 0xffffff80, v11
	v_xor_b32_e32 v0, 44, v66
	v_or_b32_e32 v188, 0x53, v66
	v_cndmask_b32_e64 v0, v0, v188, s[6:7]
	v_cmp_gt_i32_e64 s[6:7], 0, v10
	v_and_b32_e32 v3, 0xffffff80, v10
	v_or_b32_e32 v249, v0, v2
	v_xor_b32_e32 v1, 45, v66
	v_or_b32_e32 v188, 0x52, v66
	v_cndmask_b32_e64 v1, v1, v188, s[6:7]
	v_cmp_gt_i32_e64 s[6:7], 0, v13
	v_or_b32_e32 v250, v1, v3
	v_and_b32_e32 v2, 0xffffff80, v13
	v_xor_b32_e32 v0, 38, v66
	v_or_b32_e32 v188, 0x59, v66
	v_cndmask_b32_e64 v0, v0, v188, s[6:7]
	v_cmp_gt_i32_e64 s[6:7], 0, v12
	v_and_b32_e32 v3, 0xffffff80, v12
	v_or_b32_e32 v251, v0, v2
	v_xor_b32_e32 v1, 39, v66
	v_or_b32_e32 v188, 0x58, v66
	v_cndmask_b32_e64 v1, v1, v188, s[6:7]
	v_cmp_gt_i32_e64 s[6:7], 0, v15
	v_or_b32_e32 v252, v1, v3
	v_and_b32_e32 v2, 0xffffff80, v15
	v_xor_b32_e32 v0, 36, v66
	v_or_b32_e32 v188, 0x5b, v66
	v_cndmask_b32_e64 v0, v0, v188, s[6:7]
	v_cmp_gt_i32_e64 s[6:7], 0, v14
	v_and_b32_e32 v3, 0xffffff80, v14
	v_or_b32_e32 v190, v0, v2
	v_xor_b32_e32 v1, 37, v66
	v_or_b32_e32 v188, 0x5a, v66
	v_cndmask_b32_e64 v1, v1, v188, s[6:7]
	v_or_b32_e32 v195, v1, v3
	s_nop 15
	s_nop 15
	s_waitcnt vmcnt(7)
	v_mfma_f32_32x32x16_bf16 v[0:15], v[156:159], v[44:47], 0
	s_waitcnt vmcnt(6)
	v_mfma_f32_32x32x16_bf16 v[0:15], v[160:163], v[40:43], v[0:15]
	s_waitcnt vmcnt(5)
	v_mfma_f32_32x32x16_bf16 v[0:15], v[164:167], v[36:39], v[0:15]
	s_waitcnt vmcnt(4)
	v_mfma_f32_32x32x16_bf16 v[0:15], v[168:171], v[32:35], v[0:15]
	s_nop 15
	s_nop 15
	s_nop 15
	s_nop 15
	s_waitcnt vmcnt(3)
	v_mfma_f32_32x32x16_bf16 v[0:15], v[48:51], v[28:31], v[0:15]
	s_waitcnt vmcnt(2)
	v_mfma_f32_32x32x16_bf16 v[0:15], v[52:55], v[24:27], v[0:15]
	s_waitcnt vmcnt(1)
	v_mfma_f32_32x32x16_bf16 v[0:15], v[56:59], v[20:23], v[0:15]
	s_waitcnt vmcnt(0)
	v_mfma_f32_32x32x16_bf16 v[0:15], v[60:63], v[16:19], v[0:15]
	s_nop 15
	s_nop 15
	s_nop 11
	v_cmp_gt_i32_e64 s[6:7], 0, v1
	v_and_b32_e32 v1, 0xffffff80, v1
	v_and_b32_e32 v18, 0xffffff80, v0
	v_xor_b32_e32 v16, 30, v66
	v_or_b32_e32 v188, 0x61, v66
	v_cndmask_b32_e64 v16, v16, v188, s[6:7]
	v_cmp_gt_i32_e64 s[6:7], 0, v0
	v_or_b32_e32 v0, v16, v1
	s_nop 0
	v_xor_b32_e32 v17, 31, v66
	v_or_b32_e32 v188, 0x60, v66
	v_cndmask_b32_e64 v17, v17, v188, s[6:7]
	v_cmp_gt_i32_e64 s[6:7], 0, v3
	v_or_b32_e32 v1, v17, v18
	v_and_b32_e32 v3, 0xffffff80, v3
	v_xor_b32_e32 v16, 28, v66
	v_or_b32_e32 v188, 0x63, v66
	v_cndmask_b32_e64 v16, v16, v188, s[6:7]
	v_cmp_gt_i32_e64 s[6:7], 0, v2
	v_and_b32_e32 v18, 0xffffff80, v2
	v_or_b32_e32 v2, v16, v3
	v_xor_b32_e32 v17, 29, v66
	v_or_b32_e32 v188, 0x62, v66
	v_cndmask_b32_e64 v17, v17, v188, s[6:7]
	v_cmp_gt_i32_e64 s[6:7], 0, v5
	v_or_b32_e32 v3, v17, v18
	v_and_b32_e32 v5, 0xffffff80, v5
	v_xor_b32_e32 v16, 22, v66
	v_or_b32_e32 v188, 0x69, v66
	v_cndmask_b32_e64 v16, v16, v188, s[6:7]
	v_cmp_gt_i32_e64 s[6:7], 0, v4
	v_and_b32_e32 v18, 0xffffff80, v4
	v_or_b32_e32 v4, v16, v5
	v_xor_b32_e32 v17, 23, v66
	v_or_b32_e32 v188, 0x68, v66
	v_cndmask_b32_e64 v17, v17, v188, s[6:7]
	v_cmp_gt_i32_e64 s[6:7], 0, v7
	v_or_b32_e32 v5, v17, v18
	v_and_b32_e32 v7, 0xffffff80, v7
	v_xor_b32_e32 v16, 20, v66
	v_or_b32_e32 v188, 0x6b, v66
	v_cndmask_b32_e64 v16, v16, v188, s[6:7]
	v_cmp_gt_i32_e64 s[6:7], 0, v6
	v_and_b32_e32 v18, 0xffffff80, v6
	v_or_b32_e32 v6, v16, v7
	v_xor_b32_e32 v17, 21, v66
	v_or_b32_e32 v188, 0x6a, v66
	v_cndmask_b32_e64 v17, v17, v188, s[6:7]
	v_cmp_gt_i32_e64 s[6:7], 0, v9
	v_or_b32_e32 v7, v17, v18
	v_and_b32_e32 v9, 0xffffff80, v9
	v_xor_b32_e32 v16, 14, v66
	v_or_b32_e32 v188, 0x71, v66
	v_cndmask_b32_e64 v16, v16, v188, s[6:7]
	v_cmp_gt_i32_e64 s[6:7], 0, v8
	v_and_b32_e32 v18, 0xffffff80, v8
	v_or_b32_e32 v8, v16, v9
	v_xor_b32_e32 v17, 15, v66
	v_or_b32_e32 v188, 0x70, v66
	v_cndmask_b32_e64 v17, v17, v188, s[6:7]
	v_cmp_gt_i32_e64 s[6:7], 0, v11
	v_or_b32_e32 v9, v17, v18
	v_and_b32_e32 v11, 0xffffff80, v11
	v_xor_b32_e32 v16, 12, v66
	v_or_b32_e32 v188, 0x73, v66
	v_cndmask_b32_e64 v16, v16, v188, s[6:7]
	v_cmp_gt_i32_e64 s[6:7], 0, v10
	v_and_b32_e32 v18, 0xffffff80, v10
	v_or_b32_e32 v10, v16, v11
	v_xor_b32_e32 v17, 13, v66
	v_or_b32_e32 v188, 0x72, v66
	v_cndmask_b32_e64 v17, v17, v188, s[6:7]
	v_cmp_gt_i32_e64 s[6:7], 0, v13
	v_or_b32_e32 v11, v17, v18
	v_and_b32_e32 v13, 0xffffff80, v13
	v_xor_b32_e32 v16, 6, v66
	v_or_b32_e32 v188, 0x79, v66
	v_cndmask_b32_e64 v16, v16, v188, s[6:7]
	v_cmp_gt_i32_e64 s[6:7], 0, v12
	v_and_b32_e32 v18, 0xffffff80, v12
	v_or_b32_e32 v12, v16, v13
	v_xor_b32_e32 v17, 7, v66
	v_or_b32_e32 v188, 0x78, v66
	v_cndmask_b32_e64 v17, v17, v188, s[6:7]
	v_cmp_gt_i32_e64 s[6:7], 0, v15
	v_or_b32_e32 v16, v17, v18
	v_and_b32_e32 v15, 0xffffff80, v15
	v_xor_b32_e32 v13, 4, v66
	v_or_b32_e32 v188, 0x7b, v66
	v_cndmask_b32_e64 v13, v13, v188, s[6:7]
	v_cmp_gt_i32_e64 s[6:7], 0, v14
	v_and_b32_e32 v14, 0xffffff80, v14
	v_or_b32_e32 v25, v13, v15
	v_xor_b32_e32 v17, 5, v66
	v_or_b32_e32 v188, 0x7a, v66
	v_cndmask_b32_e64 v17, v17, v188, s[6:7]
	v_or_b32_e32 v28, v17, v14
	v_max_f32_e32 v13, v211, v210
	v_min_f32_e32 v14, v211, v210
	v_min_f32_e32 v15, v212, v173
	v_max_f32_e32 v17, v212, v173
	v_max_f32_e32 v18, v214, v213
	v_min_f32_e32 v19, v214, v213
	v_min_f32_e32 v20, v216, v215
	v_max_f32_e32 v21, v216, v215
	v_max_f32_e32 v22, v218, v217
	v_min_f32_e32 v23, v218, v217
	v_min_f32_e32 v24, v220, v219
	v_max_f32_e32 v26, v220, v219
	v_max_f32_e32 v27, v222, v221
	v_min_f32_e32 v29, v222, v221
	v_min_f32_e32 v30, v224, v223
	v_max_f32_e32 v31, v224, v223
	v_max_f32_e32 v32, v13, v15
	v_min_f32_e32 v13, v13, v15
	v_max_f32_e32 v15, v14, v17
	v_min_f32_e32 v14, v14, v17
	v_min_f32_e32 v17, v18, v20
	v_max_f32_e32 v18, v18, v20
	v_min_f32_e32 v20, v19, v21
	v_max_f32_e32 v19, v19, v21
	v_max_f32_e32 v21, v22, v24
	v_min_f32_e32 v22, v22, v24
	v_max_f32_e32 v24, v23, v26
	v_min_f32_e32 v23, v23, v26
	v_min_f32_e32 v26, v27, v30
	v_max_f32_e32 v27, v27, v30
	v_min_f32_e32 v30, v29, v31
	v_max_f32_e32 v29, v29, v31
	v_max_f32_e32 v31, v32, v15
	v_min_f32_e32 v15, v32, v15
	v_max_f32_e32 v32, v13, v14
	v_min_f32_e32 v13, v13, v14
	v_min_f32_e32 v14, v17, v20
	v_max_f32_e32 v17, v17, v20
	v_min_f32_e32 v20, v18, v19
	v_max_f32_e32 v18, v18, v19
	v_max_f32_e32 v19, v21, v24
	v_min_f32_e32 v21, v21, v24
	v_max_f32_e32 v24, v22, v23
	v_min_f32_e32 v22, v22, v23
	v_min_f32_e32 v23, v26, v30
	v_max_f32_e32 v26, v26, v30
	v_min_f32_e32 v30, v27, v29
	v_max_f32_e32 v27, v27, v29
	v_max_f32_e32 v29, v31, v14
	v_min_f32_e32 v14, v31, v14
	v_max_f32_e32 v31, v15, v17
	v_min_f32_e32 v15, v15, v17
	v_max_f32_e32 v17, v32, v20
	v_min_f32_e32 v20, v32, v20
	v_max_f32_e32 v32, v13, v18
	v_min_f32_e32 v13, v13, v18
	v_min_f32_e32 v18, v19, v23
	v_max_f32_e32 v19, v19, v23
	v_min_f32_e32 v23, v21, v26
	v_max_f32_e32 v21, v21, v26
	v_min_f32_e32 v26, v24, v30
	v_max_f32_e32 v24, v24, v30
	v_min_f32_e32 v30, v22, v27
	v_max_f32_e32 v22, v22, v27
	v_max_f32_e32 v27, v29, v17
	v_min_f32_e32 v17, v29, v17
	v_max_f32_e32 v29, v31, v32
	v_min_f32_e32 v31, v31, v32
	v_max_f32_e32 v32, v14, v20
	v_min_f32_e32 v14, v14, v20
	v_max_f32_e32 v20, v15, v13
	v_min_f32_e32 v13, v15, v13
	v_min_f32_e32 v15, v18, v26
	v_max_f32_e32 v18, v18, v26
	v_min_f32_e32 v26, v23, v30
	v_max_f32_e32 v23, v23, v30
	v_min_f32_e32 v30, v19, v24
	v_max_f32_e32 v19, v19, v24
	v_min_f32_e32 v24, v21, v22
	v_max_f32_e32 v21, v21, v22
	v_max_f32_e32 v22, v27, v29
	v_min_f32_e32 v27, v27, v29
	v_max_f32_e32 v29, v17, v31
	v_min_f32_e32 v17, v17, v31
	v_max_f32_e32 v31, v32, v20
	v_min_f32_e32 v20, v32, v20
	v_max_f32_e32 v32, v14, v13
	v_min_f32_e32 v13, v14, v13
	v_min_f32_e32 v14, v15, v26
	v_max_f32_e32 v15, v15, v26
	v_min_f32_e32 v26, v18, v23
	v_max_f32_e32 v18, v18, v23
	v_min_f32_e32 v23, v30, v24
	v_max_f32_e32 v24, v30, v24
	v_min_f32_e32 v30, v19, v21
	v_max_f32_e32 v19, v19, v21
	v_max_f32_e32 v21, v22, v14
	v_min_f32_e32 v14, v22, v14
	v_max_f32_e32 v22, v27, v15
	v_min_f32_e32 v15, v27, v15
	v_max_f32_e32 v27, v29, v26
	v_min_f32_e32 v26, v29, v26
	v_max_f32_e32 v29, v17, v18
	v_min_f32_e32 v17, v17, v18
	v_max_f32_e32 v18, v31, v23
	v_min_f32_e32 v23, v31, v23
	v_max_f32_e32 v31, v20, v24
	v_min_f32_e32 v20, v20, v24
	v_max_f32_e32 v24, v32, v30
	v_min_f32_e32 v30, v32, v30
	v_max_f32_e32 v32, v13, v19
	v_min_f32_e32 v13, v13, v19
	v_max_f32_e32 v19, v21, v18
	v_min_f32_e32 v18, v21, v18
	v_max_f32_e32 v21, v22, v31
	v_min_f32_e32 v22, v22, v31
	v_max_f32_e32 v31, v27, v24
	v_min_f32_e32 v24, v27, v24
	v_max_f32_e32 v27, v29, v32
	v_min_f32_e32 v29, v29, v32
	v_max_f32_e32 v32, v14, v23
	v_min_f32_e32 v14, v14, v23
	v_max_f32_e32 v23, v15, v20
	v_min_f32_e32 v15, v15, v20
	v_max_f32_e32 v20, v26, v30
	v_min_f32_e32 v26, v26, v30
	v_max_f32_e32 v30, v17, v13
	v_min_f32_e32 v13, v17, v13
	v_max_f32_e32 v17, v19, v31
	v_min_f32_e32 v19, v19, v31
	v_max_f32_e32 v33, v21, v27
	v_min_f32_e32 v21, v21, v27
	v_max_f32_e32 v34, v18, v24
	v_min_f32_e32 v18, v18, v24
	v_max_f32_e32 v24, v22, v29
	v_min_f32_e32 v22, v22, v29
	v_max_f32_e32 v35, v32, v20
	v_min_f32_e32 v32, v32, v20
	v_max_f32_e32 v20, v23, v30
	v_min_f32_e32 v36, v23, v30
	v_max_f32_e32 v37, v14, v26
	v_min_f32_e32 v38, v14, v26
	v_max_f32_e32 v14, v15, v13
	v_min_f32_e32 v13, v15, v13
	v_max_f32_e32 v31, v17, v33
	v_min_f32_e32 v29, v17, v33
	v_max_f32_e32 v30, v19, v21
	v_min_f32_e32 v26, v19, v21
	v_max_f32_e32 v27, v34, v24
	v_min_f32_e32 v23, v34, v24
	v_max_f32_e32 v24, v18, v22
	v_min_f32_e32 v21, v18, v22
	v_max_f32_e32 v22, v35, v20
	v_min_f32_e32 v19, v35, v20
	v_max_f32_e32 v20, v32, v36
	v_min_f32_e32 v17, v32, v36
	v_max_f32_e32 v18, v37, v14
	v_min_f32_e32 v14, v37, v14
	v_max_f32_e32 v15, v38, v13
	v_min_f32_e32 v13, v38, v13
	v_max_f32_e32 v32, v226, v225
	v_min_f32_e32 v33, v226, v225
	v_min_f32_e32 v34, v228, v227
	v_max_f32_e32 v35, v228, v227
	v_max_f32_e32 v36, v230, v229
	v_min_f32_e32 v37, v230, v229
	v_min_f32_e32 v38, v232, v231
	v_max_f32_e32 v39, v232, v231
	v_max_f32_e32 v40, v234, v233
	v_min_f32_e32 v41, v234, v233
	v_min_f32_e32 v42, v236, v235
	v_max_f32_e32 v43, v236, v235
	v_max_f32_e32 v44, v238, v237
	v_min_f32_e32 v45, v238, v237
	v_min_f32_e32 v46, v240, v239
	v_max_f32_e32 v47, v240, v239
	v_max_f32_e32 v48, v32, v34
	v_min_f32_e32 v32, v32, v34
	v_max_f32_e32 v34, v33, v35
	v_min_f32_e32 v33, v33, v35
	v_min_f32_e32 v35, v36, v38
	v_max_f32_e32 v36, v36, v38
	v_min_f32_e32 v38, v37, v39
	v_max_f32_e32 v37, v37, v39
	v_max_f32_e32 v39, v40, v42
	v_min_f32_e32 v40, v40, v42
	v_max_f32_e32 v42, v41, v43
	v_min_f32_e32 v41, v41, v43
	v_min_f32_e32 v43, v44, v46
	v_max_f32_e32 v44, v44, v46
	v_min_f32_e32 v46, v45, v47
	v_max_f32_e32 v45, v45, v47
	v_max_f32_e32 v47, v48, v34
	v_min_f32_e32 v34, v48, v34
	v_max_f32_e32 v48, v32, v33
	v_min_f32_e32 v32, v32, v33
	v_min_f32_e32 v33, v35, v38
	v_max_f32_e32 v35, v35, v38
	v_min_f32_e32 v38, v36, v37
	v_max_f32_e32 v36, v36, v37
	v_max_f32_e32 v37, v39, v42
	v_min_f32_e32 v39, v39, v42
	v_max_f32_e32 v42, v40, v41
	v_min_f32_e32 v40, v40, v41
	v_min_f32_e32 v41, v43, v46
	v_max_f32_e32 v43, v43, v46
	v_min_f32_e32 v46, v44, v45
	v_max_f32_e32 v44, v44, v45
	v_max_f32_e32 v45, v47, v33
	v_min_f32_e32 v33, v47, v33
	v_max_f32_e32 v47, v34, v35
	v_min_f32_e32 v34, v34, v35
	v_max_f32_e32 v35, v48, v38
	v_min_f32_e32 v38, v48, v38
	v_max_f32_e32 v48, v32, v36
	v_min_f32_e32 v32, v32, v36
	v_min_f32_e32 v36, v37, v41
	v_max_f32_e32 v37, v37, v41
	v_min_f32_e32 v41, v39, v43
	v_max_f32_e32 v39, v39, v43
	v_min_f32_e32 v43, v42, v46
	v_max_f32_e32 v42, v42, v46
	v_min_f32_e32 v46, v40, v44
	v_max_f32_e32 v40, v40, v44
	v_max_f32_e32 v44, v45, v35
	v_min_f32_e32 v35, v45, v35
	v_max_f32_e32 v45, v47, v48
	v_min_f32_e32 v47, v47, v48
	v_max_f32_e32 v48, v33, v38
	v_min_f32_e32 v33, v33, v38
	v_max_f32_e32 v38, v34, v32
	v_min_f32_e32 v32, v34, v32
	v_min_f32_e32 v34, v36, v43
	v_max_f32_e32 v36, v36, v43
	v_min_f32_e32 v43, v41, v46
	v_max_f32_e32 v41, v41, v46
	v_min_f32_e32 v46, v37, v42
	v_max_f32_e32 v37, v37, v42
	v_min_f32_e32 v42, v39, v40
	v_max_f32_e32 v39, v39, v40
	v_max_f32_e32 v40, v44, v45
	v_min_f32_e32 v44, v44, v45
	v_max_f32_e32 v45, v35, v47
	v_min_f32_e32 v35, v35, v47
	v_max_f32_e32 v47, v48, v38
	v_min_f32_e32 v38, v48, v38
	v_max_f32_e32 v48, v33, v32
	v_min_f32_e32 v32, v33, v32
	v_min_f32_e32 v33, v34, v43
	v_max_f32_e32 v34, v34, v43
	v_min_f32_e32 v43, v36, v41
	v_max_f32_e32 v36, v36, v41
	v_min_f32_e32 v41, v46, v42
	v_max_f32_e32 v42, v46, v42
	v_min_f32_e32 v46, v37, v39
	v_max_f32_e32 v37, v37, v39
	v_max_f32_e32 v39, v40, v33
	v_min_f32_e32 v33, v40, v33
	v_max_f32_e32 v40, v44, v34
	v_min_f32_e32 v34, v44, v34
	v_max_f32_e32 v44, v45, v43
	v_min_f32_e32 v43, v45, v43
	v_max_f32_e32 v45, v35, v36
	v_min_f32_e32 v35, v35, v36
	v_max_f32_e32 v36, v47, v41
	v_min_f32_e32 v41, v47, v41
	v_max_f32_e32 v47, v38, v42
	v_min_f32_e32 v38, v38, v42
	v_max_f32_e32 v42, v48, v46
	v_min_f32_e32 v46, v48, v46
	v_max_f32_e32 v48, v32, v37
	v_min_f32_e32 v32, v32, v37
	v_max_f32_e32 v37, v39, v36
	v_min_f32_e32 v36, v39, v36
	v_max_f32_e32 v39, v40, v47
	v_min_f32_e32 v40, v40, v47
	v_max_f32_e32 v47, v44, v42
	v_min_f32_e32 v42, v44, v42
	v_max_f32_e32 v44, v45, v48
	v_min_f32_e32 v45, v45, v48
	v_max_f32_e32 v48, v33, v41
	v_min_f32_e32 v33, v33, v41
	v_max_f32_e32 v41, v34, v38
	v_min_f32_e32 v34, v34, v38
	v_max_f32_e32 v38, v43, v46
	v_min_f32_e32 v43, v43, v46
	v_max_f32_e32 v46, v35, v32
	v_min_f32_e32 v32, v35, v32
	v_max_f32_e32 v35, v37, v47
	v_min_f32_e32 v37, v37, v47
	v_max_f32_e32 v47, v39, v44
	v_min_f32_e32 v39, v39, v44
	v_max_f32_e32 v44, v36, v42
	v_min_f32_e32 v42, v36, v42
	v_max_f32_e32 v49, v40, v45
	v_min_f32_e32 v40, v40, v45
	v_max_f32_e32 v45, v48, v38
	v_min_f32_e32 v48, v48, v38
	v_max_f32_e32 v50, v41, v46
	v_min_f32_e32 v41, v41, v46
	v_max_f32_e32 v46, v33, v43
	v_min_f32_e32 v43, v33, v43
	v_max_f32_e32 v51, v34, v32
	v_min_f32_e32 v52, v34, v32
	v_max_f32_e32 v32, v35, v47
	v_min_f32_e32 v33, v35, v47
	v_max_f32_e32 v34, v37, v39
	v_min_f32_e32 v35, v37, v39
	v_max_f32_e32 v36, v44, v49
	v_min_f32_e32 v37, v44, v49
	v_max_f32_e32 v38, v42, v40
	v_min_f32_e32 v39, v42, v40
	v_max_f32_e32 v40, v45, v50
	v_min_f32_e32 v42, v45, v50
	v_max_f32_e32 v44, v48, v41
	v_min_f32_e32 v41, v48, v41
	v_max_f32_e32 v45, v46, v51
	v_min_f32_e32 v46, v46, v51
	v_max_f32_e32 v47, v43, v52
	v_min_f32_e32 v43, v43, v52
	v_max_f32_e32 v48, v183, v182
	v_min_f32_e32 v49, v183, v182
	v_min_f32_e32 v50, v242, v241
	v_max_f32_e32 v51, v242, v241
	v_max_f32_e32 v52, v244, v243
	v_min_f32_e32 v53, v244, v243
	v_min_f32_e32 v54, v246, v245
	v_max_f32_e32 v55, v246, v245
	v_max_f32_e32 v56, v248, v247
	v_min_f32_e32 v57, v248, v247
	v_min_f32_e32 v58, v250, v249
	v_max_f32_e32 v59, v250, v249
	v_max_f32_e32 v60, v252, v251
	v_min_f32_e32 v61, v252, v251
	v_min_f32_e32 v62, v195, v190
	v_max_f32_e32 v63, v195, v190
	v_max_f32_e32 v173, v48, v50
	v_min_f32_e32 v48, v48, v50
	v_max_f32_e32 v50, v49, v51
	v_min_f32_e32 v49, v49, v51
	v_min_f32_e32 v51, v52, v54
	v_max_f32_e32 v52, v52, v54
	v_min_f32_e32 v54, v53, v55
	v_max_f32_e32 v53, v53, v55
	v_max_f32_e32 v55, v56, v58
	v_min_f32_e32 v56, v56, v58
	v_max_f32_e32 v58, v57, v59
	v_min_f32_e32 v57, v57, v59
	v_min_f32_e32 v59, v60, v62
	v_max_f32_e32 v60, v60, v62
	v_min_f32_e32 v62, v61, v63
	v_max_f32_e32 v61, v61, v63
	v_max_f32_e32 v63, v173, v50
	v_min_f32_e32 v50, v173, v50
	v_max_f32_e32 v173, v48, v49
	v_min_f32_e32 v48, v48, v49
	v_min_f32_e32 v49, v51, v54
	v_max_f32_e32 v51, v51, v54
	v_min_f32_e32 v54, v52, v53
	v_max_f32_e32 v52, v52, v53
	v_max_f32_e32 v53, v55, v58
	v_min_f32_e32 v55, v55, v58
	v_max_f32_e32 v58, v56, v57
	v_min_f32_e32 v56, v56, v57
	v_min_f32_e32 v57, v59, v62
	v_max_f32_e32 v59, v59, v62
	v_min_f32_e32 v62, v60, v61
	v_max_f32_e32 v60, v60, v61
	v_max_f32_e32 v61, v63, v49
	v_min_f32_e32 v49, v63, v49
	v_max_f32_e32 v63, v50, v51
	v_min_f32_e32 v50, v50, v51
	v_max_f32_e32 v51, v173, v54
	v_min_f32_e32 v54, v173, v54
	v_max_f32_e32 v173, v48, v52
	v_min_f32_e32 v48, v48, v52
	v_min_f32_e32 v52, v53, v57
	v_max_f32_e32 v53, v53, v57
	v_min_f32_e32 v57, v55, v59
	v_max_f32_e32 v55, v55, v59
	v_min_f32_e32 v59, v58, v62
	v_max_f32_e32 v58, v58, v62
	v_min_f32_e32 v62, v56, v60
	v_max_f32_e32 v56, v56, v60
	v_max_f32_e32 v60, v61, v51
	v_min_f32_e32 v51, v61, v51
	v_max_f32_e32 v61, v63, v173
	v_min_f32_e32 v63, v63, v173
	v_max_f32_e32 v173, v49, v54
	v_min_f32_e32 v49, v49, v54
	v_max_f32_e32 v54, v50, v48
	v_min_f32_e32 v48, v50, v48
	v_min_f32_e32 v50, v52, v59
	v_max_f32_e32 v52, v52, v59
	v_min_f32_e32 v59, v57, v62
	v_max_f32_e32 v57, v57, v62
	v_min_f32_e32 v62, v53, v58
	v_max_f32_e32 v53, v53, v58
	v_min_f32_e32 v58, v55, v56
	v_max_f32_e32 v55, v55, v56
	v_max_f32_e32 v56, v60, v61
	v_min_f32_e32 v60, v60, v61
	v_max_f32_e32 v61, v51, v63
	v_min_f32_e32 v51, v51, v63
	v_max_f32_e32 v63, v173, v54
	v_min_f32_e32 v54, v173, v54
	v_max_f32_e32 v173, v49, v48
	v_min_f32_e32 v48, v49, v48
	v_min_f32_e32 v49, v50, v59
	v_max_f32_e32 v50, v50, v59
	v_min_f32_e32 v59, v52, v57
	v_max_f32_e32 v52, v52, v57
	v_min_f32_e32 v57, v62, v58
	v_max_f32_e32 v58, v62, v58
	v_min_f32_e32 v62, v53, v55
	v_max_f32_e32 v53, v53, v55
	v_max_f32_e32 v55, v56, v49
	v_min_f32_e32 v49, v56, v49
	v_max_f32_e32 v56, v60, v50
	v_min_f32_e32 v50, v60, v50
	v_max_f32_e32 v60, v61, v59
	v_min_f32_e32 v59, v61, v59
	v_max_f32_e32 v61, v51, v52
	v_min_f32_e32 v51, v51, v52
	v_max_f32_e32 v52, v63, v57
	v_min_f32_e32 v57, v63, v57
	v_max_f32_e32 v63, v54, v58
	v_min_f32_e32 v54, v54, v58
	v_max_f32_e32 v58, v173, v62
	v_min_f32_e32 v62, v173, v62
	v_max_f32_e32 v173, v48, v53
	v_min_f32_e32 v48, v48, v53
	v_max_f32_e32 v53, v55, v52
	v_min_f32_e32 v52, v55, v52
	v_max_f32_e32 v55, v56, v63
	v_min_f32_e32 v56, v56, v63
	v_max_f32_e32 v63, v60, v58
	v_min_f32_e32 v58, v60, v58
	v_max_f32_e32 v60, v61, v173
	v_min_f32_e32 v61, v61, v173
	v_max_f32_e32 v173, v49, v57
	v_min_f32_e32 v49, v49, v57
	v_max_f32_e32 v57, v50, v54
	v_min_f32_e32 v50, v50, v54
	v_max_f32_e32 v54, v59, v62
	v_min_f32_e32 v59, v59, v62
	v_max_f32_e32 v62, v51, v48
	v_min_f32_e32 v48, v51, v48
	v_max_f32_e32 v51, v53, v63
	v_min_f32_e32 v53, v53, v63
	v_max_f32_e32 v63, v55, v60
	v_min_f32_e32 v55, v55, v60
	v_max_f32_e32 v60, v52, v58
	v_min_f32_e32 v52, v52, v58
	v_max_f32_e32 v58, v56, v61
	v_min_f32_e32 v56, v56, v61
	v_max_f32_e32 v61, v173, v54
	v_min_f32_e32 v54, v173, v54
	v_max_f32_e32 v173, v57, v62
	v_min_f32_e32 v57, v57, v62
	v_max_f32_e32 v62, v49, v59
	v_min_f32_e32 v49, v49, v59
	v_max_f32_e32 v59, v50, v48
	v_min_f32_e32 v48, v50, v48
	v_max_f32_e32 v50, v51, v63
	v_min_f32_e32 v51, v51, v63
	v_max_f32_e32 v63, v53, v55
	v_min_f32_e32 v53, v53, v55
	v_max_f32_e32 v55, v60, v58
	v_min_f32_e32 v58, v60, v58
	v_max_f32_e32 v60, v52, v56
	v_min_f32_e32 v52, v52, v56
	v_max_f32_e32 v56, v61, v173
	v_min_f32_e32 v61, v61, v173
	v_max_f32_e32 v173, v54, v57
	v_min_f32_e32 v54, v54, v57
	v_max_f32_e32 v57, v62, v59
	v_min_f32_e32 v59, v62, v59
	v_max_f32_e32 v62, v49, v48
	v_min_f32_e32 v48, v49, v48
	v_max_f32_e32 v49, v1, v0
	v_min_f32_e32 v0, v1, v0
	v_min_f32_e32 v1, v3, v2
	v_max_f32_e32 v2, v3, v2
	v_max_f32_e32 v3, v5, v4
	v_min_f32_e32 v4, v5, v4
	v_min_f32_e32 v5, v7, v6
	v_max_f32_e32 v6, v7, v6
	v_max_f32_e32 v7, v9, v8
	v_min_f32_e32 v8, v9, v8
	v_min_f32_e32 v9, v11, v10
	v_max_f32_e32 v10, v11, v10
	v_max_f32_e32 v11, v16, v12
	v_min_f32_e32 v12, v16, v12
	v_min_f32_e32 v16, v28, v25
	v_max_f32_e32 v25, v28, v25
	v_max_f32_e32 v28, v49, v1
	v_min_f32_e32 v1, v49, v1
	v_max_f32_e32 v49, v0, v2
	v_min_f32_e32 v0, v0, v2
	v_min_f32_e32 v2, v3, v5
	v_max_f32_e32 v3, v3, v5
	v_min_f32_e32 v5, v4, v6
	v_max_f32_e32 v4, v4, v6
	v_max_f32_e32 v6, v7, v9
	v_min_f32_e32 v7, v7, v9
	v_max_f32_e32 v9, v8, v10
	v_min_f32_e32 v8, v8, v10
	v_min_f32_e32 v10, v11, v16
	v_max_f32_e32 v11, v11, v16
	v_min_f32_e32 v16, v12, v25
	v_max_f32_e32 v12, v12, v25
	v_max_f32_e32 v25, v28, v49
	v_min_f32_e32 v28, v28, v49
	v_max_f32_e32 v49, v1, v0
	v_min_f32_e32 v0, v1, v0
	v_min_f32_e32 v1, v2, v5
	v_max_f32_e32 v2, v2, v5
	v_min_f32_e32 v5, v3, v4
	v_max_f32_e32 v3, v3, v4
	v_max_f32_e32 v4, v6, v9
	v_min_f32_e32 v6, v6, v9
	v_max_f32_e32 v9, v7, v8
	v_min_f32_e32 v7, v7, v8
	v_min_f32_e32 v8, v10, v16
	v_max_f32_e32 v10, v10, v16
	v_min_f32_e32 v16, v11, v12
	v_max_f32_e32 v11, v11, v12
	v_max_f32_e32 v12, v25, v1
	v_min_f32_e32 v1, v25, v1
	v_max_f32_e32 v25, v28, v2
	v_min_f32_e32 v2, v28, v2
	v_max_f32_e32 v28, v49, v5
	v_min_f32_e32 v5, v49, v5
	v_max_f32_e32 v49, v0, v3
	v_min_f32_e32 v0, v0, v3
	v_min_f32_e32 v3, v4, v8
	v_max_f32_e32 v4, v4, v8
	v_min_f32_e32 v8, v6, v10
	v_max_f32_e32 v6, v6, v10
	v_min_f32_e32 v10, v9, v16
	v_max_f32_e32 v9, v9, v16
	v_min_f32_e32 v16, v7, v11
	v_max_f32_e32 v7, v7, v11
	v_max_f32_e32 v11, v12, v28
	v_min_f32_e32 v12, v12, v28
	v_max_f32_e32 v28, v25, v49
	v_min_f32_e32 v25, v25, v49
	v_max_f32_e32 v49, v1, v5
	v_min_f32_e32 v1, v1, v5
	v_max_f32_e32 v5, v2, v0
	v_min_f32_e32 v0, v2, v0
	v_min_f32_e32 v2, v3, v10
	v_max_f32_e32 v3, v3, v10
	v_min_f32_e32 v10, v8, v16
	v_max_f32_e32 v8, v8, v16
	v_min_f32_e32 v16, v4, v9
	v_max_f32_e32 v4, v4, v9
	v_min_f32_e32 v9, v6, v7
	v_max_f32_e32 v6, v6, v7
	v_max_f32_e32 v7, v11, v28
	v_min_f32_e32 v11, v11, v28
	v_max_f32_e32 v28, v12, v25
	v_min_f32_e32 v12, v12, v25
	v_max_f32_e32 v25, v49, v5
	v_min_f32_e32 v5, v49, v5
	v_max_f32_e32 v49, v1, v0
	v_min_f32_e32 v0, v1, v0
	v_min_f32_e32 v1, v2, v10
	v_max_f32_e32 v2, v2, v10
	v_min_f32_e32 v10, v3, v8
	v_max_f32_e32 v3, v3, v8
	v_min_f32_e32 v8, v16, v9
	v_max_f32_e32 v9, v16, v9
	v_min_f32_e32 v16, v4, v6
	v_max_f32_e32 v4, v4, v6
	v_max_f32_e32 v6, v7, v1
	v_min_f32_e32 v1, v7, v1
	v_max_f32_e32 v7, v11, v2
	v_min_f32_e32 v2, v11, v2
	v_max_f32_e32 v11, v28, v10
	v_min_f32_e32 v10, v28, v10
	v_max_f32_e32 v28, v12, v3
	v_min_f32_e32 v3, v12, v3
	v_max_f32_e32 v12, v25, v8
	v_min_f32_e32 v8, v25, v8
	v_max_f32_e32 v25, v5, v9
	v_min_f32_e32 v5, v5, v9
	v_max_f32_e32 v9, v49, v16
	v_min_f32_e32 v16, v49, v16
	v_max_f32_e32 v49, v0, v4
	v_min_f32_e32 v0, v0, v4
	v_max_f32_e32 v4, v6, v12
	v_min_f32_e32 v6, v6, v12
	v_max_f32_e32 v12, v7, v25
	v_min_f32_e32 v7, v7, v25
	v_max_f32_e32 v25, v11, v9
	v_min_f32_e32 v9, v11, v9
	v_max_f32_e32 v11, v28, v49
	v_min_f32_e32 v28, v28, v49
	v_max_f32_e32 v49, v1, v8
	v_min_f32_e32 v1, v1, v8
	v_max_f32_e32 v8, v2, v5
	v_min_f32_e32 v2, v2, v5
	v_max_f32_e32 v5, v10, v16
	v_min_f32_e32 v10, v10, v16
	v_max_f32_e32 v16, v3, v0
	v_min_f32_e32 v0, v3, v0
	v_max_f32_e32 v3, v4, v25
	v_min_f32_e32 v4, v4, v25
	v_max_f32_e32 v25, v12, v11
	v_min_f32_e32 v11, v12, v11
	v_max_f32_e32 v12, v6, v9
	v_min_f32_e32 v6, v6, v9
	v_max_f32_e32 v9, v7, v28
	v_min_f32_e32 v7, v7, v28
	v_max_f32_e32 v28, v49, v5
	v_min_f32_e32 v5, v49, v5
	v_max_f32_e32 v49, v8, v16
	v_min_f32_e32 v8, v8, v16
	v_max_f32_e32 v16, v1, v10
	v_min_f32_e32 v1, v1, v10
	v_max_f32_e32 v10, v2, v0
	v_min_f32_e32 v0, v2, v0
	v_max_f32_e32 v2, v3, v25
	v_min_f32_e32 v3, v3, v25
	v_max_f32_e32 v25, v4, v11
	v_min_f32_e32 v4, v4, v11
	v_max_f32_e32 v11, v12, v9
	v_min_f32_e32 v9, v12, v9
	v_max_f32_e32 v12, v6, v7
	v_min_f32_e32 v6, v6, v7
	v_max_f32_e32 v7, v28, v49
	v_min_f32_e32 v28, v28, v49
	v_max_f32_e32 v49, v5, v8
	v_min_f32_e32 v5, v5, v8
	v_max_f32_e32 v8, v16, v10
	v_min_f32_e32 v10, v16, v10
	v_max_f32_e32 v16, v1, v0
	v_min_f32_e32 v0, v1, v0
	v_max_f32_e32 v1, v31, v43
	v_max_f32_e32 v29, v29, v47
	v_max_f32_e32 v30, v30, v46
	v_max_f32_e32 v26, v26, v45
	v_max_f32_e32 v27, v27, v41
	v_max_f32_e32 v23, v23, v44
	v_max_f32_e32 v24, v24, v42
	v_max_f32_e32 v21, v21, v40
	v_max_f32_e32 v22, v22, v39
	v_max_f32_e32 v19, v19, v38
	v_max_f32_e32 v20, v20, v37
	v_max_f32_e32 v17, v17, v36
	v_max_f32_e32 v18, v18, v35
	v_max_f32_e32 v14, v14, v34
	v_max_f32_e32 v15, v15, v33
	v_max_f32_e32 v13, v13, v32
	v_max_f32_e32 v31, v1, v22
	v_min_f32_e32 v1, v1, v22
	v_max_f32_e32 v22, v29, v19
	v_min_f32_e32 v19, v29, v19
	v_max_f32_e32 v29, v30, v20
	v_min_f32_e32 v20, v30, v20
	v_max_f32_e32 v30, v26, v17
	v_min_f32_e32 v17, v26, v17
	v_max_f32_e32 v26, v27, v18
	v_min_f32_e32 v18, v27, v18
	v_max_f32_e32 v27, v23, v14
	v_min_f32_e32 v14, v23, v14
	v_max_f32_e32 v23, v24, v15
	v_min_f32_e32 v15, v24, v15
	v_max_f32_e32 v24, v21, v13
	v_min_f32_e32 v13, v21, v13
	v_max_f32_e32 v21, v31, v26
	v_min_f32_e32 v26, v31, v26
	v_max_f32_e32 v31, v22, v27
	v_min_f32_e32 v22, v22, v27
	v_max_f32_e32 v27, v29, v23
	v_min_f32_e32 v23, v29, v23
	v_max_f32_e32 v29, v30, v24
	v_min_f32_e32 v24, v30, v24
	v_max_f32_e32 v30, v1, v18
	v_min_f32_e32 v1, v1, v18
	v_max_f32_e32 v18, v19, v14
	v_min_f32_e32 v14, v19, v14
	v_max_f32_e32 v19, v20, v15
	v_min_f32_e32 v15, v20, v15
	v_max_f32_e32 v20, v17, v13
	v_min_f32_e32 v13, v17, v13
	v_max_f32_e32 v17, v21, v27
	v_min_f32_e32 v21, v21, v27
	v_max_f32_e32 v27, v31, v29
	v_min_f32_e32 v29, v31, v29
	v_max_f32_e32 v31, v26, v23
	v_min_f32_e32 v23, v26, v23
	v_max_f32_e32 v26, v22, v24
	v_min_f32_e32 v22, v22, v24
	v_max_f32_e32 v24, v30, v19
	v_min_f32_e32 v19, v30, v19
	v_max_f32_e32 v30, v18, v20
	v_min_f32_e32 v18, v18, v20
	v_max_f32_e32 v20, v1, v15
	v_min_f32_e32 v1, v1, v15
	v_max_f32_e32 v15, v14, v13
	v_min_f32_e32 v13, v14, v13
	v_max_f32_e32 v14, v17, v27
	v_min_f32_e32 v17, v17, v27
	v_max_f32_e32 v27, v21, v29
	v_min_f32_e32 v21, v21, v29
	v_max_f32_e32 v29, v31, v26
	v_min_f32_e32 v26, v31, v26
	v_max_f32_e32 v31, v23, v22
	v_min_f32_e32 v22, v23, v22
	v_max_f32_e32 v23, v24, v30
	v_min_f32_e32 v24, v24, v30
	v_max_f32_e32 v30, v19, v18
	v_min_f32_e32 v18, v19, v18
	v_max_f32_e32 v19, v20, v15
	v_min_f32_e32 v15, v20, v15
	v_max_f32_e32 v20, v1, v13
	v_min_f32_e32 v1, v1, v13
	v_max_f32_e32 v0, v50, v0
	v_max_f32_e32 v13, v51, v16
	v_max_f32_e32 v10, v63, v10
	v_max_f32_e32 v8, v53, v8
	v_max_f32_e32 v5, v55, v5
	v_max_f32_e32 v16, v58, v49
	v_max_f32_e32 v28, v60, v28
	v_max_f32_e32 v7, v52, v7
	v_max_f32_e32 v6, v56, v6
	v_max_f32_e32 v12, v61, v12
	v_max_f32_e32 v9, v173, v9
	v_max_f32_e32 v11, v54, v11
	v_max_f32_e32 v4, v57, v4
	v_max_f32_e32 v25, v59, v25
	v_max_f32_e32 v3, v62, v3
	v_max_f32_e32 v2, v48, v2
	v_max_f32_e32 v32, v0, v6
	v_min_f32_e32 v0, v0, v6
	v_max_f32_e32 v6, v13, v12
	v_min_f32_e32 v12, v13, v12
	v_max_f32_e32 v13, v10, v9
	v_min_f32_e32 v9, v10, v9
	v_max_f32_e32 v10, v8, v11
	v_min_f32_e32 v8, v8, v11
	v_max_f32_e32 v11, v5, v4
	v_min_f32_e32 v4, v5, v4
	v_max_f32_e32 v5, v16, v25
	v_min_f32_e32 v16, v16, v25
	v_max_f32_e32 v25, v28, v3
	v_min_f32_e32 v3, v28, v3
	v_max_f32_e32 v28, v7, v2
	v_min_f32_e32 v2, v7, v2
	v_max_f32_e32 v7, v32, v11
	v_min_f32_e32 v11, v32, v11
	v_max_f32_e32 v32, v6, v5
	v_min_f32_e32 v5, v6, v5
	v_max_f32_e32 v6, v13, v25
	v_min_f32_e32 v13, v13, v25
	v_max_f32_e32 v25, v10, v28
	v_min_f32_e32 v10, v10, v28
	v_max_f32_e32 v28, v0, v4
	v_min_f32_e32 v0, v0, v4
	v_max_f32_e32 v4, v12, v16
	v_min_f32_e32 v12, v12, v16
	v_max_f32_e32 v16, v9, v3
	v_min_f32_e32 v3, v9, v3
	v_max_f32_e32 v9, v8, v2
	v_min_f32_e32 v2, v8, v2
	v_max_f32_e32 v8, v7, v6
	v_min_f32_e32 v6, v7, v6
	v_max_f32_e32 v7, v32, v25
	v_min_f32_e32 v25, v32, v25
	v_max_f32_e32 v32, v11, v13
	v_min_f32_e32 v11, v11, v13
	v_max_f32_e32 v13, v5, v10
	v_min_f32_e32 v5, v5, v10
	v_max_f32_e32 v10, v28, v16
	v_min_f32_e32 v16, v28, v16
	v_max_f32_e32 v28, v4, v9
	v_min_f32_e32 v4, v4, v9
	v_max_f32_e32 v9, v0, v3
	v_min_f32_e32 v0, v0, v3
	v_max_f32_e32 v3, v12, v2
	v_min_f32_e32 v2, v12, v2
	v_max_f32_e32 v12, v8, v7
	v_min_f32_e32 v7, v8, v7
	v_max_f32_e32 v8, v6, v25
	v_min_f32_e32 v6, v6, v25
	v_max_f32_e32 v25, v32, v13
	v_min_f32_e32 v13, v32, v13
	v_max_f32_e32 v32, v11, v5
	v_min_f32_e32 v5, v11, v5
	v_max_f32_e32 v11, v10, v28
	v_min_f32_e32 v10, v10, v28
	v_max_f32_e32 v28, v16, v4
	v_min_f32_e32 v4, v16, v4
	v_max_f32_e32 v16, v9, v3
	v_min_f32_e32 v3, v9, v3
	v_max_f32_e32 v9, v0, v2
	v_min_f32_e32 v0, v0, v2
	v_max_f32_e32 v0, v14, v0
	v_max_f32_e32 v2, v17, v9
	v_max_f32_e32 v3, v27, v3
	v_max_f32_e32 v9, v21, v16
	v_max_f32_e32 v4, v29, v4
	v_max_f32_e32 v14, v26, v28
	v_max_f32_e32 v10, v31, v10
	v_max_f32_e32 v11, v22, v11
	v_max_f32_e32 v5, v23, v5
	v_max_f32_e32 v16, v24, v32
	v_max_f32_e32 v13, v30, v13
	v_max_f32_e32 v17, v18, v25
	v_max_f32_e32 v6, v19, v6
	v_max_f32_e32 v8, v15, v8
	v_max_f32_e32 v7, v20, v7
	v_max_f32_e32 v1, v1, v12
	v_max_f32_e32 v12, v0, v5
	v_min_f32_e32 v0, v0, v5
	v_max_f32_e32 v5, v2, v16
	v_min_f32_e32 v2, v2, v16
	v_max_f32_e32 v15, v3, v13
	v_min_f32_e32 v3, v3, v13
	v_max_f32_e32 v13, v9, v17
	v_min_f32_e32 v9, v9, v17
	v_max_f32_e32 v16, v4, v6
	v_min_f32_e32 v4, v4, v6
	v_max_f32_e32 v6, v14, v8
	v_min_f32_e32 v8, v14, v8
	v_max_f32_e32 v14, v10, v7
	v_min_f32_e32 v7, v10, v7
	v_max_f32_e32 v10, v11, v1
	v_min_f32_e32 v1, v11, v1
	v_max_f32_e32 v11, v12, v16
	v_min_f32_e32 v12, v12, v16
	v_max_f32_e32 v16, v5, v6
	v_min_f32_e32 v5, v5, v6
	v_max_f32_e32 v6, v15, v14
	v_min_f32_e32 v14, v15, v14
	v_max_f32_e32 v15, v13, v10
	v_min_f32_e32 v10, v13, v10
	v_max_f32_e32 v13, v0, v4
	v_min_f32_e32 v0, v0, v4
	v_max_f32_e32 v4, v2, v8
	v_min_f32_e32 v2, v2, v8
	v_max_f32_e32 v8, v3, v7
	v_min_f32_e32 v3, v3, v7
	v_max_f32_e32 v7, v9, v1
	v_min_f32_e32 v1, v9, v1
	v_max_f32_e32 v9, v11, v6
	v_min_f32_e32 v6, v11, v6
	v_max_f32_e32 v11, v16, v15
	v_min_f32_e32 v15, v16, v15
	v_max_f32_e32 v16, v12, v14
	v_min_f32_e32 v12, v12, v14
	v_max_f32_e32 v14, v5, v10
	v_min_f32_e32 v5, v5, v10
	v_max_f32_e32 v10, v13, v8
	v_min_f32_e32 v8, v13, v8
	v_max_f32_e32 v13, v4, v7
	v_min_f32_e32 v4, v4, v7
	v_max_f32_e32 v7, v0, v3
	v_min_f32_e32 v0, v0, v3
	v_max_f32_e32 v3, v2, v1
	v_min_f32_e32 v1, v2, v1
	v_max_f32_e32 v2, v9, v11
	v_min_f32_e32 v9, v9, v11
	v_max_f32_e32 v11, v6, v15
	v_min_f32_e32 v6, v6, v15
	v_max_f32_e32 v15, v16, v14
	v_min_f32_e32 v14, v16, v14
	v_max_f32_e32 v16, v12, v5
	v_min_f32_e32 v5, v12, v5
	v_max_f32_e32 v12, v10, v13
	v_min_f32_e32 v10, v10, v13
	v_max_f32_e32 v13, v8, v4
	v_min_f32_e32 v4, v8, v4
	v_max_f32_e32 v8, v7, v3
	v_min_f32_e32 v3, v7, v3
	v_max_f32_e32 v7, v0, v1
	v_min_f32_e32 v0, v0, v1
	v_mov_b32_e32 v27, v0
	s_nop 1
	v_permlane32_swap_b32 v27, v27
	v_mov_b32_e32 v29, v7
	s_nop 1
	v_permlane32_swap_b32 v29, v29
	v_mov_b32_e32 v31, v3
	s_nop 1
	v_permlane32_swap_b32 v31, v31
	v_mov_b32_e32 v30, v8
	s_nop 1
	v_permlane32_swap_b32 v30, v30
	v_mov_b32_e32 v28, v4
	s_nop 1
	v_permlane32_swap_b32 v28, v28
	v_mov_b32_e32 v26, v13
	s_nop 1
	v_permlane32_swap_b32 v26, v26
	s_waitcnt lgkmcnt(5)
	v_mov_b32_e32 v1, v2
	s_nop 1
	v_permlane32_swap_b32 v1, v1
	v_mov_b32_e32 v25, v10
	s_nop 1
	v_permlane32_swap_b32 v25, v25
	v_max_f32_e32 v2, v2, v27
	s_waitcnt lgkmcnt(6)
	v_mov_b32_e32 v17, v9
	s_nop 1
	v_permlane32_swap_b32 v17, v17
	v_mov_b32_e32 v24, v12
	s_nop 1
	v_permlane32_swap_b32 v24, v24
	v_max_f32_e32 v9, v9, v29
	s_waitcnt lgkmcnt(7)
	v_mov_b32_e32 v18, v11
	s_nop 1
	v_permlane32_swap_b32 v18, v18
	v_mov_b32_e32 v23, v5
	s_nop 1
	v_permlane32_swap_b32 v23, v23
	v_max_f32_e32 v11, v11, v31
	s_waitcnt lgkmcnt(8)
	v_mov_b32_e32 v19, v6
	s_nop 1
	v_permlane32_swap_b32 v19, v19
	v_mov_b32_e32 v22, v16
	s_nop 1
	v_permlane32_swap_b32 v22, v22
	v_max_f32_e32 v6, v6, v30
	s_waitcnt lgkmcnt(9)
	v_mov_b32_e32 v20, v15
	s_nop 1
	v_permlane32_swap_b32 v20, v20
	v_mov_b32_e32 v21, v14
	s_nop 1
	v_permlane32_swap_b32 v21, v21
	v_max_f32_e32 v15, v15, v28
	s_waitcnt lgkmcnt(10)
	v_max_f32_e32 v14, v14, v26
	s_waitcnt lgkmcnt(8)
	v_max_f32_e32 v16, v16, v25
	s_waitcnt lgkmcnt(6)
	v_max_f32_e32 v5, v5, v24
	s_waitcnt lgkmcnt(4)
	v_max_f32_e32 v12, v12, v23
	s_waitcnt lgkmcnt(2)
	v_max_f32_e32 v10, v10, v22
	s_waitcnt lgkmcnt(0)
	v_max_f32_e32 v13, v13, v21
	v_max_f32_e32 v4, v4, v20
	v_max_f32_e32 v8, v8, v19
	v_max_f32_e32 v3, v3, v18
	v_max_f32_e32 v7, v7, v17
	v_max_f32_e32 v0, v0, v1
	v_max_f32_e32 v1, v2, v12
	v_min_f32_e32 v2, v2, v12
	v_max_f32_e32 v12, v9, v10
	v_min_f32_e32 v9, v9, v10
	v_max_f32_e32 v10, v11, v13
	v_min_f32_e32 v11, v11, v13
	v_max_f32_e32 v13, v6, v4
	v_min_f32_e32 v4, v6, v4
	v_max_f32_e32 v6, v15, v8
	v_min_f32_e32 v8, v15, v8
	v_max_f32_e32 v15, v14, v3
	v_min_f32_e32 v3, v14, v3
	v_max_f32_e32 v14, v16, v7
	v_min_f32_e32 v7, v16, v7
	v_max_f32_e32 v16, v5, v0
	v_min_f32_e32 v0, v5, v0
	v_max_f32_e32 v5, v1, v6
	v_min_f32_e32 v1, v1, v6
	v_max_f32_e32 v6, v12, v15
	v_min_f32_e32 v12, v12, v15
	v_max_f32_e32 v15, v10, v14
	v_min_f32_e32 v10, v10, v14
	v_max_f32_e32 v14, v13, v16
	v_min_f32_e32 v13, v13, v16
	v_max_f32_e32 v16, v2, v8
	v_min_f32_e32 v2, v2, v8
	v_max_f32_e32 v8, v9, v3
	v_min_f32_e32 v3, v9, v3
	v_max_f32_e32 v9, v11, v7
	v_min_f32_e32 v7, v11, v7
	v_max_f32_e32 v11, v4, v0
	v_min_f32_e32 v0, v4, v0
	v_max_f32_e32 v4, v5, v15
	v_min_f32_e32 v5, v5, v15
	v_max_f32_e32 v15, v6, v14
	v_min_f32_e32 v6, v6, v14
	v_max_f32_e32 v14, v1, v10
	v_min_f32_e32 v1, v1, v10
	v_max_f32_e32 v10, v12, v13
	v_min_f32_e32 v12, v12, v13
	v_max_f32_e32 v13, v16, v9
	v_min_f32_e32 v9, v16, v9
	v_max_f32_e32 v16, v8, v11
	v_min_f32_e32 v8, v8, v11
	v_max_f32_e32 v11, v2, v7
	v_min_f32_e32 v2, v2, v7
	v_max_f32_e32 v7, v3, v0
	v_min_f32_e32 v0, v3, v0
	v_max_f32_e32 v3, v4, v15
	v_min_f32_e32 v4, v4, v15
	v_max_f32_e32 v15, v5, v6
	v_min_f32_e32 v5, v5, v6
	v_max_f32_e32 v6, v14, v10
	v_min_f32_e32 v10, v14, v10
	v_max_f32_e32 v14, v1, v12
	v_min_f32_e32 v1, v1, v12
	v_max_f32_e32 v12, v13, v16
	v_min_f32_e32 v13, v13, v16
	v_max_f32_e32 v16, v9, v8
	v_min_f32_e32 v8, v9, v8
	v_max_f32_e32 v9, v11, v7
	v_min_f32_e32 v7, v11, v7
	v_max_f32_e32 v11, v2, v0
	v_min_f32_e32 v0, v2, v0
	v_lshl_add_u32 v2, s8, 12, v207
	ds_write2st64_b32 v2, v3, v4 offset1:1
	ds_write2st64_b32 v2, v15, v5 offset0:2 offset1:3
	ds_write2st64_b32 v2, v6, v10 offset0:4 offset1:5
	ds_write2st64_b32 v2, v14, v1 offset0:6 offset1:7
	ds_write2st64_b32 v2, v12, v13 offset0:8 offset1:9
	ds_write2st64_b32 v2, v16, v8 offset0:10 offset1:11
	ds_write2st64_b32 v2, v9, v7 offset0:12 offset1:13
	ds_write2st64_b32 v2, v11, v0 offset0:14 offset1:15
	s_mov_b64 s[6:7], 0
	s_mov_b32 s8, 1
	s_cbranch_vccz .LBB0_704
	ds_read2st64_b32 v[0:1], v207 offset1:1
	ds_read2st64_b32 v[2:3], v207 offset0:2 offset1:3
	ds_read2st64_b32 v[4:5], v207 offset0:4 offset1:5
	ds_read2st64_b32 v[6:7], v207 offset0:6 offset1:7
	ds_read2st64_b32 v[16:17], v207 offset0:16 offset1:17
	ds_read2st64_b32 v[18:19], v207 offset0:18 offset1:19
	ds_read2st64_b32 v[20:21], v207 offset0:20 offset1:21
	ds_read2st64_b32 v[22:23], v207 offset0:22 offset1:23
	ds_read2st64_b32 v[8:9], v207 offset0:8 offset1:9
	ds_read2st64_b32 v[10:11], v207 offset0:10 offset1:11
	ds_read2st64_b32 v[12:13], v207 offset0:12 offset1:13
	ds_read2st64_b32 v[14:15], v207 offset0:14 offset1:15
	ds_read2st64_b32 v[24:25], v207 offset0:24 offset1:25
	ds_read2st64_b32 v[26:27], v207 offset0:26 offset1:27
	ds_read2st64_b32 v[28:29], v207 offset0:28 offset1:29
	ds_read2st64_b32 v[30:31], v207 offset0:30 offset1:31
	s_and_saveexec_b64 s[8:9], s[38:39]
	s_cbranch_execz .LBB0_696
	s_waitcnt lgkmcnt(0)
	v_and_b32_e32 v49, 0xffffff80, v30
	v_and_b32_e32 v48, 0xffffff80, v0
	v_and_b32_e32 v39, 0xffffff80, v19
	v_and_b32_e32 v38, 0xffffff80, v20
	v_pk_add_f32 v[52:53], v[38:39], v[48:49] op_sel:[1,0] op_sel_hi:[0,1]
	v_cmp_gt_i32_e32 vcc, 0, v52
	v_bfrev_b32_e32 v43, 0.5
	s_movk_i32 s12, 0xff00
	v_cndmask_b32_e64 v43, v43, 3, vcc
	v_and_b32_e32 v42, 0xffffff80, v23
	v_and_or_b32 v56, v52, s12, v43
	v_mov_b32_e32 v43, v38
	v_pk_add_f32 v[52:53], v[48:49], v[42:43] op_sel_hi:[0,1]
	v_cmp_gt_i32_e32 vcc, 0, v53
	v_mov_b32_e32 v54, 0xfb
	v_and_b32_e32 v41, 0xffffff80, v22
	v_cndmask_b32_e64 v54, v54, 4, vcc
	v_and_b32_e32 v40, 0xffffff80, v21
	v_and_or_b32 v53, v53, s12, v54
	v_cmp_gt_i32_e32 vcc, 0, v52
	v_mov_b32_e32 v54, 0xf8
	v_mov_b32_e32 v58, 0xf9
	v_cndmask_b32_e64 v57, v54, 7, vcc
	v_pk_add_f32 v[54:55], v[48:49], v[40:41] op_sel_hi:[0,1]
	v_cmp_gt_i32_e32 vcc, 0, v55
	v_mov_b32_e32 v59, 0xfa
	v_and_b32_e32 v55, 0xffffff00, v55
	v_cndmask_b32_e64 v58, v58, 6, vcc
	v_cmp_gt_i32_e32 vcc, 0, v54
	v_and_b32_e32 v54, 0xffffff00, v54
	v_and_b32_e32 v52, 0xffffff00, v52
	v_cndmask_b32_e64 v59, v59, 5, vcc
	v_or_b32_e32 v55, v58, v55
	v_or_b32_e32 v54, v59, v54
	v_or_b32_e32 v52, v57, v52
	v_writelane_b32 v255, s8, 44
	v_min_f32_e32 v57, v55, v52
	v_max_f32_e32 v58, v53, v54
	v_min_f32_e32 v53, v53, v54
	v_max_f32_e32 v52, v55, v52
	v_writelane_b32 v255, s9, 45
	v_and_b32_e32 v45, 0xffffff80, v24
	v_and_b32_e32 v44, 0xffffff80, v27
	v_min_f32_e32 v59, v58, v57
	v_min_f32_e32 v54, v53, v52
	v_max_f32_e32 v57, v58, v57
	v_max_f32_e32 v52, v53, v52
	v_pk_add_f32 v[44:45], v[48:49], v[44:45] op_sel_hi:[0,1]
	v_and_b32_e32 v47, 0xffffff80, v26
	v_min_f32_e32 v58, v57, v52
	v_max_f32_e32 v57, v57, v52
	v_cmp_gt_i32_e32 vcc, 0, v45
	v_mov_b32_e32 v52, 0xf7
	v_and_b32_e32 v46, 0xffffff80, v25
	v_cndmask_b32_e64 v52, v52, 8, vcc
	v_and_or_b32 v45, v45, s12, v52
	v_cmp_gt_i32_e32 vcc, 0, v44
	v_mov_b32_e32 v52, 0xf4
	v_pk_add_f32 v[46:47], v[48:49], v[46:47] op_sel_hi:[0,1]
	v_cndmask_b32_e64 v52, v52, 11, vcc
	v_cmp_gt_i32_e32 vcc, 0, v47
	v_mov_b32_e32 v53, 0xf5
	v_min_f32_e32 v55, v59, v54
	v_max_f32_e32 v59, v59, v54
	v_cndmask_b32_e64 v53, v53, 10, vcc
	v_cmp_gt_i32_e32 vcc, 0, v46
	v_mov_b32_e32 v54, 0xf6
	v_and_b32_e32 v47, 0xffffff00, v47
	v_cndmask_b32_e64 v54, v54, 9, vcc
	v_and_b32_e32 v46, 0xffffff00, v46
	v_and_b32_e32 v44, 0xffffff00, v44
	v_or_b32_e32 v47, v53, v47
	v_or_b32_e32 v46, v54, v46
	v_or_b32_e32 v44, v52, v44
	v_and_b32_e32 v51, 0xffffff80, v29
	v_and_b32_e32 v50, 0xffffff80, v28
	v_writelane_b32 v255, s11, 46
	v_min_f32_e32 v52, v47, v44
	v_max_f32_e32 v53, v45, v46
	v_min_f32_e32 v46, v45, v46
	v_max_f32_e32 v47, v47, v44
	v_pk_add_f32 v[44:45], v[48:49], v[50:51] op_sel_hi:[0,1]
	v_cmp_gt_i32_e64 s[10:11], 0, v45
	v_mov_b32_e32 v50, 0xf2
	v_mov_b32_e32 v51, 0xf3
	v_cndmask_b32_e64 v50, v50, 13, s[10:11]
	v_cmp_gt_i32_e64 s[10:11], 0, v44
	v_and_b32_e32 v45, 0xffffff00, v45
	v_and_b32_e32 v44, 0xffffff00, v44
	v_cndmask_b32_e64 v51, v51, 12, s[10:11]
	v_or_b32_e32 v50, v50, v45
	v_or_b32_e32 v51, v51, v44
	v_and_b32_e32 v45, 0xffffff80, v31
	v_mov_b32_e32 v44, v49
	v_pk_add_f32 v[44:45], v[48:49], v[44:45] op_sel_hi:[0,1]
	v_cmp_gt_i32_e64 s[42:43], 0, v45
	v_mov_b32_e32 v249, 0xf0
	v_mov_b32_e32 v173, 0xf1
	v_cndmask_b32_e64 v63, v249, 15, s[42:43]
	v_cmp_gt_i32_e64 s[42:43], 0, v44
	v_and_b32_e32 v45, 0xffffff00, v45
	v_and_b32_e32 v44, 0xffffff00, v44
	v_cndmask_b32_e64 v173, v173, 14, s[42:43]
	v_or_b32_e32 v45, v63, v45
	v_or_b32_e32 v44, v173, v44
	v_max_f32_e32 v62, v51, v50
	v_min_f32_e32 v63, v44, v45
	v_min_f32_e32 v50, v51, v50
	v_max_f32_e32 v44, v44, v45
	v_max_f32_e32 v54, v53, v52
	v_max_f32_e32 v60, v46, v47
	v_min_f32_e32 v173, v62, v63
	v_min_f32_e32 v45, v50, v44
	v_min_f32_e32 v51, v53, v52
	v_min_f32_e32 v46, v46, v47
	v_max_f32_e32 v52, v62, v63
	v_max_f32_e32 v44, v50, v44
	v_max_f32_e32 v61, v54, v60
	v_min_f32_e32 v178, v173, v45
	v_max_f32_e32 v47, v51, v46
	v_min_f32_e32 v50, v52, v44
	v_min_f32_e32 v54, v54, v60
	v_max_f32_e32 v45, v173, v45
	v_min_f32_e32 v46, v51, v46
	v_max_f32_e32 v44, v52, v44
	v_min_f32_e32 v179, v61, v178
	v_min_f32_e32 v53, v47, v50
	v_min_f32_e32 v60, v54, v45
	v_min_f32_e32 v52, v46, v44
	v_max_f32_e32 v61, v61, v178
	v_max_f32_e32 v47, v47, v50
	v_max_f32_e32 v45, v54, v45
	v_max_f32_e32 v44, v46, v44
	v_min_f32_e32 v62, v179, v53
	v_min_f32_e32 v63, v60, v52
	v_min_f32_e32 v50, v61, v47
	v_min_f32_e32 v46, v45, v44
	v_max_f32_e32 v53, v179, v53
	v_max_f32_e32 v52, v60, v52
	v_max_f32_e32 v47, v61, v47
	v_max_f32_e32 v44, v45, v44
	v_min_f32_e32 v60, v53, v52
	v_min_f32_e32 v61, v47, v44
	v_max_f32_e32 v52, v53, v52
	v_max_f32_e32 v53, v47, v44
	v_and_b32_e32 v44, 0xffffff80, v1
	v_add_f32_e32 v45, v39, v44
	v_min_f32_e32 v51, v62, v63
	v_min_f32_e32 v173, v50, v46
	v_max_f32_e32 v62, v62, v63
	v_max_f32_e32 v63, v50, v46
	v_cmp_gt_i32_e32 vcc, 0, v45
	v_mov_b32_e32 v46, 0xec
	v_mov_b32_e32 v47, 0xe9
	v_cndmask_b32_e64 v46, v46, 19, vcc
	v_and_or_b32 v45, v45, s12, v46
	v_pk_add_f32 v[42:43], v[44:45], v[42:43] op_sel_hi:[0,1]
	v_cmp_gt_i32_e32 vcc, 0, v43
	v_mov_b32_e32 v46, 0xeb
	v_pk_add_f32 v[40:41], v[44:45], v[40:41] op_sel_hi:[0,1]
	v_cndmask_b32_e64 v46, v46, 20, vcc
	v_and_or_b32 v43, v43, s12, v46
	v_cmp_gt_i32_e32 vcc, 0, v42
	v_mov_b32_e32 v46, 0xe8
	v_mov_b32_e32 v50, 0xea
	v_cndmask_b32_e64 v46, v46, 23, vcc
	v_cmp_gt_i32_e32 vcc, 0, v41
	v_and_b32_e32 v41, 0xffffff00, v41
	v_and_b32_e32 v42, 0xffffff00, v42
	v_cndmask_b32_e64 v47, v47, 22, vcc
	v_cmp_gt_i32_e32 vcc, 0, v40
	v_and_b32_e32 v40, 0xffffff00, v40
	v_or_b32_e32 v41, v47, v41
	v_cndmask_b32_e64 v50, v50, 21, vcc
	v_or_b32_e32 v40, v50, v40
	v_or_b32_e32 v42, v46, v42
	v_and_b32_e32 v182, 0xffffff80, v3
	v_min_f32_e32 v46, v41, v42
	v_max_f32_e32 v47, v43, v40
	v_min_f32_e32 v40, v43, v40
	v_max_f32_e32 v41, v41, v42
	v_and_b32_e32 v37, 0xffffff80, v4
	v_max_f32_e32 v43, v47, v46
	v_min_f32_e32 v42, v40, v41
	v_max_f32_e32 v40, v40, v41
	v_min_f32_e32 v50, v47, v46
	v_and_b32_e32 v46, 0xffffff80, v2
	v_and_b32_e32 v36, 0xffffff80, v18
	v_min_f32_e32 v179, v43, v40
	v_max_f32_e32 v180, v43, v40
	v_pk_add_f32 v[40:41], v[46:47], v[38:39] op_sel_hi:[0,1]
	v_cmp_gt_i32_e32 vcc, 0, v41
	v_mov_b32_e32 v38, 0xdc
	v_and_b32_e32 v35, 0xffffff80, v7
	v_cndmask_b32_e64 v38, v38, 35, vcc
	v_and_or_b32 v41, v41, s12, v38
	v_cmp_gt_i32_e32 vcc, 0, v40
	v_mov_b32_e32 v38, 0xdb
	v_and_b32_e32 v34, 0xffffff80, v17
	v_cndmask_b32_e64 v38, v38, 36, vcc
	v_and_or_b32 v181, v40, s12, v38
	v_add_f32_e32 v38, v39, v182
	v_cmp_gt_i32_e32 vcc, 0, v38
	v_mov_b32_e32 v39, 0xcc
	s_nop 0
	v_cndmask_b32_e64 v39, v39, 51, vcc
	v_and_or_b32 v54, v38, s12, v39
	v_pk_add_f32 v[38:39], v[48:49], v[36:37]
	v_min_f32_e32 v178, v50, v42
	v_cmp_gt_i32_e32 vcc, 0, v38
	v_bfrev_b32_e32 v39, -0.5
	v_max_f32_e32 v50, v50, v42
	v_cndmask_b32_e64 v39, v39, 2, vcc
	v_and_or_b32 v38, v38, s12, v39
	v_mov_b32_e32 v39, 0xed
	v_and_b32_e32 v43, 0xffffff80, v6
	v_min_f32_e32 v183, v38, v56
	v_max_f32_e32 v56, v38, v56
	v_add_f32_e32 v38, v36, v44
	v_cmp_gt_i32_e32 vcc, 0, v38
	v_and_b32_e32 v42, 0xffffff80, v5
	v_and_b32_e32 v33, 0xffffff80, v14
	v_cndmask_b32_e64 v39, v39, 18, vcc
	v_and_or_b32 v38, v38, s12, v39
	v_mov_b32_e32 v39, 0xdd
	v_and_b32_e32 v32, 0xffffff80, v16
	v_min_f32_e32 v190, v38, v45
	v_max_f32_e32 v195, v38, v45
	v_add_f32_e32 v38, v36, v46
	v_cmp_gt_i32_e32 vcc, 0, v38
	v_mov_b32_e32 v45, 0x61
	v_mov_b32_e32 v234, 0xef
	v_cndmask_b32_e64 v39, v39, 34, vcc
	v_and_or_b32 v38, v38, s12, v39
	v_mov_b32_e32 v39, 0xcd
	v_mov_b32_e32 v241, 0xdf
	v_min_f32_e32 v209, v38, v41
	v_max_f32_e32 v210, v38, v41
	v_add_f32_e32 v38, v36, v182
	v_cmp_gt_i32_e32 vcc, 0, v38
	v_mov_b32_e32 v41, 0x42
	v_mov_b32_e32 v244, 0xcf
	v_cndmask_b32_e64 v39, v39, 50, vcc
	v_and_or_b32 v40, v38, s12, v39
	v_pk_add_f32 v[38:39], v[36:37], v[36:37] op_sel:[1,0] op_sel_hi:[0,1]
	v_cmp_gt_i32_e32 vcc, 0, v38
	v_mov_b32_e32 v39, 0xbd
	v_and_b32_e32 v47, 0xffffff80, v8
	v_cndmask_b32_e32 v39, v39, v41, vcc
	v_and_or_b32 v41, v38, s12, v39
	v_pk_add_f32 v[38:39], v[48:49], v[34:35]
	v_pk_add_f32 v[48:49], v[48:49], v[32:33]
	v_cmp_gt_i32_e32 vcc, 0, v38
	v_mov_b32_e32 v39, 0xfe
	s_mov_b32 s28, 0xff61b1e6
	v_cndmask_b32_e64 v39, v39, 1, vcc
	v_and_or_b32 v211, v38, s12, v39
	v_add_f32_e32 v38, v34, v44
	v_cmp_gt_i32_e32 vcc, 0, v38
	v_mov_b32_e32 v39, 0xee
	v_add_f32_e32 v44, v32, v44
	v_cndmask_b32_e64 v39, v39, 17, vcc
	v_and_or_b32 v212, v38, s12, v39
	v_add_f32_e32 v38, v34, v46
	v_cmp_gt_i32_e32 vcc, 0, v38
	v_mov_b32_e32 v39, 0xde
	v_add_f32_e32 v46, v32, v46
	v_cndmask_b32_e64 v39, v39, 33, vcc
	v_and_or_b32 v213, v38, s12, v39
	v_add_f32_e32 v38, v34, v182
	v_cmp_gt_i32_e32 vcc, 0, v38
	v_mov_b32_e32 v39, 0xce
	v_add_f32_e32 v182, v32, v182
	v_cndmask_b32_e64 v39, v39, 49, vcc
	v_and_or_b32 v38, v38, s12, v39
	v_cmp_gt_i32_e64 s[74:75], 0, v46
	v_cmp_gt_i32_e64 s[84:85], 0, v182
	v_min_f32_e32 v219, v38, v40
	v_max_f32_e32 v220, v38, v40
	v_pk_add_f32 v[38:39], v[36:37], v[34:35] op_sel:[1,0] op_sel_hi:[0,1]
	v_cmp_gt_i32_e32 vcc, 0, v38
	v_mov_b32_e32 v39, 0xbe
	v_mov_b32_e32 v40, 0x41
	v_cndmask_b32_e32 v39, v39, v40, vcc
	v_and_or_b32 v38, v38, s12, v39
	v_mov_b32_e32 v40, v35
	v_cndmask_b32_e64 v241, v241, 32, s[74:75]
	v_min_f32_e32 v215, v38, v41
	v_max_f32_e32 v216, v38, v41
	v_pk_add_f32 v[38:39], v[34:35], v[42:43]
	v_mov_b32_e32 v41, v43
	v_pk_add_f32 v[40:41], v[34:35], v[40:41] op_sel_hi:[0,1]
	v_cmp_gt_i32_e32 vcc, 0, v38
	v_mov_b32_e32 v34, 0xae
	v_mov_b32_e32 v39, 0x51
	v_cndmask_b32_e32 v34, v34, v39, vcc
	v_cmp_gt_i32_e32 vcc, 0, v41
	v_mov_b32_e32 v39, 0x9e
	v_and_b32_e32 v38, 0xffffff00, v38
	v_cndmask_b32_e32 v39, v39, v45, vcc
	v_or_b32_e32 v218, v34, v38
	v_cmp_gt_i32_e32 vcc, 0, v40
	v_mov_b32_e32 v34, 0x8e
	v_mov_b32_e32 v38, 0x71
	v_cndmask_b32_e32 v34, v34, v38, vcc
	v_and_or_b32 v214, v40, s12, v34
	v_cmp_gt_i32_e32 vcc, 0, v48
	v_mov_b32_e32 v34, 0xff
	v_cndmask_b32_e64 v244, v244, 48, s[84:85]
	v_cndmask_b32_e64 v34, v34, 0, vcc
	v_and_or_b32 v34, v48, s12, v34
	v_and_or_b32 v46, v46, s12, v241
	v_and_or_b32 v182, v182, s12, v244
	v_max_f32_e32 v48, v34, v211
	v_min_f32_e32 v34, v34, v211
	v_max_f32_e32 v49, v48, v183
	v_max_f32_e32 v211, v34, v56
	v_min_f32_e32 v48, v48, v183
	v_min_f32_e32 v34, v34, v56
	v_max_f32_e32 v221, v49, v211
	v_max_f32_e32 v56, v48, v34
	v_min_f32_e32 v49, v49, v211
	v_min_f32_e32 v34, v48, v34
	v_max_f32_e32 v222, v221, v55
	v_max_f32_e32 v183, v56, v58
	v_max_f32_e32 v211, v49, v59
	v_max_f32_e32 v48, v34, v57
	v_min_f32_e32 v55, v221, v55
	v_min_f32_e32 v56, v56, v58
	v_min_f32_e32 v49, v49, v59
	v_min_f32_e32 v34, v34, v57
	v_max_f32_e32 v241, v46, v213
	v_max_f32_e32 v58, v55, v56
	v_max_f32_e32 v57, v49, v34
	v_min_f32_e32 v55, v55, v56
	v_min_f32_e32 v34, v49, v34
	v_min_f32_e32 v46, v46, v213
	v_max_f32_e32 v244, v181, v182
	v_max_f32_e32 v49, v55, v34
	v_min_f32_e32 v34, v55, v34
	v_cmp_gt_i32_e64 s[6:7], 0, v44
	v_min_f32_e32 v181, v181, v182
	s_nop 0
	v_cndmask_b32_e64 v234, v234, 16, s[6:7]
	v_and_or_b32 v44, v44, s12, v234
	v_max_f32_e32 v234, v44, v212
	v_min_f32_e32 v44, v44, v212
	v_max_f32_e32 v235, v234, v190
	v_max_f32_e32 v212, v44, v195
	v_min_f32_e32 v190, v234, v190
	v_min_f32_e32 v44, v44, v195
	v_max_f32_e32 v242, v241, v209
	v_max_f32_e32 v213, v46, v210
	v_min_f32_e32 v245, v244, v219
	v_min_f32_e32 v182, v181, v220
	v_min_f32_e32 v209, v241, v209
	v_min_f32_e32 v46, v46, v210
	v_max_f32_e32 v219, v244, v219
	v_max_f32_e32 v181, v181, v220
	v_max_f32_e32 v59, v58, v57
	v_min_f32_e32 v57, v58, v57
	v_max_f32_e32 v236, v235, v212
	v_max_f32_e32 v195, v190, v44
	v_min_f32_e32 v212, v235, v212
	v_min_f32_e32 v44, v190, v44
	v_max_f32_e32 v243, v242, v213
	v_min_f32_e32 v246, v245, v182
	v_max_f32_e32 v210, v209, v46
	v_min_f32_e32 v220, v219, v181
	v_min_f32_e32 v213, v242, v213
	v_max_f32_e32 v182, v245, v182
	v_min_f32_e32 v46, v209, v46
	v_max_f32_e32 v181, v219, v181
	v_max_f32_e32 v237, v236, v178
	v_max_f32_e32 v234, v195, v179
	v_max_f32_e32 v235, v212, v50
	v_max_f32_e32 v190, v44, v180
	v_min_f32_e32 v247, v243, v246
	v_min_f32_e32 v241, v210, v220
	v_min_f32_e32 v242, v213, v182
	v_min_f32_e32 v209, v46, v181
	v_min_f32_e32 v178, v236, v178
	v_min_f32_e32 v179, v195, v179
	v_min_f32_e32 v50, v212, v50
	v_min_f32_e32 v44, v44, v180
	v_max_f32_e32 v236, v243, v246
	v_max_f32_e32 v210, v210, v220
	v_max_f32_e32 v182, v213, v182
	v_max_f32_e32 v46, v46, v181
	v_max_f32_e32 v223, v222, v183
	v_max_f32_e32 v224, v211, v48
	v_min_f32_e32 v183, v222, v183
	v_min_f32_e32 v48, v211, v48
	v_max_f32_e32 v238, v237, v234
	v_max_f32_e32 v239, v235, v190
	v_min_f32_e32 v244, v247, v241
	v_min_f32_e32 v219, v242, v209
	v_max_f32_e32 v195, v178, v179
	v_max_f32_e32 v180, v50, v44
	v_min_f32_e32 v220, v236, v210
	v_min_f32_e32 v181, v182, v46
	v_min_f32_e32 v234, v237, v234
	v_min_f32_e32 v190, v235, v190
	v_max_f32_e32 v237, v247, v241
	v_max_f32_e32 v209, v242, v209
	v_min_f32_e32 v178, v178, v179
	v_min_f32_e32 v44, v50, v44
	v_max_f32_e32 v50, v236, v210
	v_max_f32_e32 v46, v182, v46
	v_max_f32_e32 v225, v223, v224
	v_max_f32_e32 v211, v183, v48
	v_min_f32_e32 v223, v223, v224
	v_min_f32_e32 v48, v183, v48
	v_max_f32_e32 v240, v238, v239
	v_min_f32_e32 v245, v244, v219
	v_max_f32_e32 v212, v195, v180
	v_min_f32_e32 v213, v220, v181
	v_max_f32_e32 v235, v234, v190
	v_min_f32_e32 v241, v237, v209
	v_max_f32_e32 v179, v178, v44
	v_min_f32_e32 v182, v50, v46
	v_min_f32_e32 v238, v238, v239
	v_max_f32_e32 v219, v244, v219
	v_min_f32_e32 v180, v195, v180
	v_max_f32_e32 v181, v220, v181
	v_min_f32_e32 v190, v234, v190
	v_max_f32_e32 v209, v237, v209
	v_min_f32_e32 v44, v178, v44
	v_max_f32_e32 v46, v50, v46
	v_max_f32_e32 v226, v225, v51
	v_max_f32_e32 v221, v59, v173
	v_max_f32_e32 v222, v211, v60
	v_max_f32_e32 v56, v49, v61
	v_max_f32_e32 v224, v223, v62
	v_max_f32_e32 v58, v57, v63
	v_max_f32_e32 v183, v48, v52
	v_max_f32_e32 v55, v34, v53
	v_min_f32_e32 v248, v240, v245
	v_min_f32_e32 v243, v212, v213
	v_min_f32_e32 v242, v235, v241
	v_min_f32_e32 v210, v179, v182
	v_min_f32_e32 v239, v238, v219
	v_min_f32_e32 v195, v180, v181
	v_min_f32_e32 v234, v190, v209
	v_min_f32_e32 v178, v44, v46
	v_max_f32_e32 v227, v226, v221
	v_max_f32_e32 v228, v222, v56
	v_max_f32_e32 v230, v224, v58
	v_max_f32_e32 v231, v183, v55
	v_min_f32_e32 v246, v248, v243
	v_min_f32_e32 v236, v242, v210
	v_min_f32_e32 v220, v239, v195
	v_min_f32_e32 v237, v234, v178
	v_max_f32_e32 v229, v227, v228
	v_max_f32_e32 v232, v230, v231
	v_min_f32_e32 v247, v246, v236
	v_min_f32_e32 v244, v220, v237
	v_min_f32_e32 v51, v225, v51
	v_min_f32_e32 v59, v59, v173
	v_min_f32_e32 v60, v211, v60
	v_min_f32_e32 v61, v49, v61
	v_min_f32_e32 v62, v223, v62
	v_min_f32_e32 v57, v57, v63
	v_min_f32_e32 v48, v48, v52
	v_min_f32_e32 v34, v34, v53
	v_max_f32_e32 v63, v240, v245
	v_max_f32_e32 v212, v212, v213
	v_max_f32_e32 v235, v235, v241
	v_max_f32_e32 v179, v179, v182
	v_max_f32_e32 v219, v238, v219
	v_max_f32_e32 v180, v180, v181
	v_max_f32_e32 v190, v190, v209
	v_max_f32_e32 v44, v44, v46
	v_max_f32_e32 v233, v229, v232
	v_min_f32_e32 v50, v247, v244
	v_max_f32_e32 v173, v51, v59
	v_max_f32_e32 v211, v60, v61
	v_max_f32_e32 v223, v62, v57
	v_max_f32_e32 v53, v48, v34
	v_min_f32_e32 v213, v63, v212
	v_min_f32_e32 v182, v235, v179
	v_min_f32_e32 v181, v219, v180
	v_min_f32_e32 v46, v190, v44
	v_min_f32_e32 v227, v227, v228
	v_min_f32_e32 v228, v230, v231
	v_max_f32_e32 v230, v246, v236
	v_max_f32_e32 v220, v220, v237
	v_max_f32_e32 v50, v233, v50
	v_max_f32_e32 v44, v190, v44
	v_max_f32_e32 v225, v173, v211
	v_max_f32_e32 v233, v223, v53
	v_min_f32_e32 v240, v213, v182
	v_min_f32_e32 v209, v181, v46
	v_min_f32_e32 v221, v226, v221
	v_min_f32_e32 v222, v222, v56
	v_min_f32_e32 v224, v224, v58
	v_min_f32_e32 v183, v183, v55
	v_max_f32_e32 v241, v248, v243
	v_max_f32_e32 v210, v242, v210
	v_max_f32_e32 v195, v239, v195
	v_max_f32_e32 v234, v234, v178
	v_min_f32_e32 v51, v51, v59
	v_min_f32_e32 v59, v60, v61
	v_min_f32_e32 v57, v62, v57
	v_min_f32_e32 v34, v48, v34
	v_max_f32_e32 v60, v63, v212
	v_max_f32_e32 v62, v235, v179
	v_max_f32_e32 v58, v227, v228
	v_min_f32_e32 v63, v230, v220
	v_min_f32_e32 v211, v173, v211
	v_min_f32_e32 v223, v223, v53
	v_max_f32_e32 v213, v213, v182
	v_max_f32_e32 v46, v181, v46
	v_max_f32_e32 v226, v221, v222
	v_max_f32_e32 v238, v224, v183
	v_max_f32_e32 v243, v51, v59
	v_max_f32_e32 v245, v57, v34
	v_min_f32_e32 v179, v60, v62
	v_max_f32_e32 v63, v58, v63
	v_max_f32_e32 v53, v211, v223
	v_min_f32_e32 v58, v213, v46
	v_min_f32_e32 v181, v221, v222
	v_min_f32_e32 v221, v224, v183
	v_max_f32_e32 v222, v241, v210
	v_max_f32_e32 v224, v195, v234
	v_min_f32_e32 v51, v51, v59
	v_min_f32_e32 v59, v57, v34
	v_max_f32_e32 v231, v60, v62
	v_min_f32_e32 v57, v229, v232
	v_max_f32_e32 v62, v247, v244
	v_min_f32_e32 v239, v195, v234
	v_min_f32_e32 v242, v241, v210
	v_max_f32_e32 v212, v219, v180
	v_max_f32_e32 v178, v53, v58
	v_max_f32_e32 v53, v181, v221
	v_min_f32_e32 v173, v222, v224
	v_max_f32_e32 v183, v57, v62
	v_min_f32_e32 v57, v225, v233
	v_max_f32_e32 v62, v240, v209
	v_min_f32_e32 v219, v212, v44
	v_max_f32_e32 v180, v53, v173
	v_max_f32_e32 v190, v57, v62
	v_min_f32_e32 v57, v226, v238
	v_max_f32_e32 v173, v242, v239
	v_max_f32_e32 v55, v226, v238
	v_min_f32_e32 v56, v242, v239
	v_max_f32_e32 v210, v230, v220
	v_max_f32_e32 v195, v57, v173
	v_min_f32_e32 v57, v243, v245
	v_max_f32_e32 v173, v179, v219
	v_max_f32_e32 v55, v55, v56
	v_min_f32_e32 v56, v179, v219
	v_min_f32_e32 v179, v227, v228
	v_min_f32_e32 v52, v240, v209
	v_max_f32_e32 v209, v57, v173
	v_max_f32_e32 v46, v213, v46
	v_max_f32_e32 v44, v212, v44
	v_max_f32_e32 v210, v179, v210
	v_min_f32_e32 v179, v211, v223
	v_max_f32_e32 v211, v179, v46
	v_min_f32_e32 v46, v181, v221
	v_max_f32_e32 v181, v222, v224
	v_min_f32_e32 v53, v231, v44
	v_max_f32_e32 v44, v231, v44
	v_max_f32_e32 v212, v46, v181
	v_min_f32_e32 v46, v51, v59
	v_max_f32_e32 v34, v51, v59
	v_pk_add_f32 v[36:37], v[36:37], v[32:33] op_sel:[1,0] op_sel_hi:[0,1]
	v_mov_b32_e32 v37, 0xbf
	v_max_f32_e32 v213, v46, v44
	v_cmp_gt_i32_e32 vcc, 0, v36
	v_mov_b32_e32 v221, 0x50
	v_and_b32_e32 v41, 0xffffff00, v41
	v_cndmask_b32_e64 v37, v37, 64, vcc
	v_and_or_b32 v36, v36, s12, v37
	v_or_b32_e32 v217, v39, v41
	v_max_f32_e32 v49, v225, v233
	v_max_f32_e32 v44, v54, v36
	v_min_f32_e32 v54, v54, v36
	v_pk_add_f32 v[36:37], v[32:33], v[42:43] op_sel_hi:[0,1]
	v_cmp_gt_i32_e64 s[68:69], 0, v37
	v_mov_b32_e32 v42, 0x9f
	v_mov_b32_e32 v43, 0x60
	v_cndmask_b32_e64 v42, v42, v43, s[68:69]
	v_cmp_gt_i32_e64 s[68:69], 0, v36
	v_mov_b32_e32 v43, 0xaf
	v_and_b32_e32 v37, 0xffffff00, v37
	v_cndmask_b32_e64 v43, v43, v221, s[68:69]
	v_and_b32_e32 v36, 0xffffff00, v36
	v_or_b32_e32 v37, v42, v37
	v_or_b32_e32 v36, v43, v36
	v_min_f32_e32 v42, v37, v217
	v_max_f32_e32 v43, v36, v218
	v_max_f32_e32 v37, v37, v217
	v_min_f32_e32 v36, v36, v218
	v_max_f32_e32 v46, v44, v215
	v_max_f32_e32 v219, v54, v216
	v_min_f32_e32 v221, v43, v42
	v_min_f32_e32 v217, v36, v37
	v_max_f32_e32 v42, v43, v42
	v_max_f32_e32 v36, v36, v37
	v_max_f32_e32 v220, v46, v219
	v_min_f32_e32 v44, v44, v215
	v_min_f32_e32 v54, v54, v216
	v_min_f32_e32 v219, v46, v219
	v_mov_b32_e32 v46, v35
	v_min_f32_e32 v216, v42, v36
	v_max_f32_e32 v225, v42, v36
	v_pk_add_f32 v[36:37], v[32:33], v[46:47] op_sel_hi:[0,1]
	v_and_b32_e32 v45, 0xffffff80, v9
	v_max_f32_e32 v215, v44, v54
	v_min_f32_e32 v54, v44, v54
	v_mov_b32_e32 v44, v35
	v_cmp_gt_i32_e32 vcc, 0, v37
	v_mov_b32_e32 v35, 0x7f
	v_pk_add_f32 v[42:43], v[32:33], v[44:45] op_sel_hi:[0,1]
	v_cndmask_b32_e32 v35, v35, v196, vcc
	v_cmp_gt_i32_e32 vcc, 0, v36
	v_mov_b32_e32 v47, 0x8f
	v_mov_b32_e32 v45, 0x6f
	v_cndmask_b32_e32 v44, v47, v198, vcc
	v_cmp_gt_i32_e32 vcc, 0, v43
	v_mov_b32_e32 v46, 0x90
	v_and_b32_e32 v37, 0xffffff00, v37
	v_and_b32_e32 v36, 0xffffff00, v36
	v_cndmask_b32_e32 v45, v45, v46, vcc
	v_and_b32_e32 v43, 0xffffff00, v43
	v_cmp_gt_i32_e32 vcc, 0, v42
	v_or_b32_e32 v35, v35, v37
	v_or_b32_e32 v36, v44, v36
	v_or_b32_e32 v37, v45, v43
	v_and_b32_e32 v41, 0xffffff80, v10
	v_and_b32_e32 v40, 0xffffff80, v13
	v_cndmask_b32_e32 v46, v47, v198, vcc
	v_cmp_lt_f32_e32 vcc, v37, v35
	v_cmp_lt_f32_e64 s[8:9], v214, v36
	v_and_b32_e32 v39, 0xffffff80, v12
	v_cndmask_b32_e32 v43, v35, v37, vcc
	v_cndmask_b32_e64 v45, v36, v214, s[8:9]
	v_cndmask_b32_e32 v35, v37, v35, vcc
	v_pk_add_f32 v[36:37], v[32:33], v[40:41] op_sel_hi:[0,1]
	v_cmp_gt_i32_e64 s[80:81], 0, v37
	v_mov_b32_e32 v40, 0x5f
	v_mov_b32_e32 v41, 0xa0
	v_and_b32_e32 v38, 0xffffff80, v11
	v_cndmask_b32_e64 v40, v40, v41, s[80:81]
	v_and_b32_e32 v42, 0xffffff00, v42
	v_and_or_b32 v37, v37, s12, v40
	v_cmp_gt_i32_e64 s[80:81], 0, v36
	v_mov_b32_e32 v40, 0xd0
	v_pk_add_f32 v[38:39], v[32:33], v[38:39] op_sel_hi:[0,1]
	v_or_b32_e32 v42, v46, v42
	v_cndmask_b32_e64 v40, 47, v40, s[80:81]
	v_cmp_gt_i32_e64 s[80:81], 0, v39
	v_mov_b32_e32 v41, 0xc0
	v_cndmask_b32_e64 v42, v214, v42, s[8:9]
	v_cndmask_b32_e64 v41, 63, v41, s[80:81]
	v_cmp_gt_i32_e64 s[80:81], 0, v38
	v_mov_b32_e32 v214, 0x4f
	v_mov_b32_e32 v229, 0xb0
	v_cndmask_b32_e64 v214, v214, v229, s[80:81]
	v_and_b32_e32 v39, 0xffffff00, v39
	v_and_b32_e32 v38, 0xffffff00, v38
	v_and_b32_e32 v36, 0xffffff00, v36
	v_or_b32_e32 v39, v41, v39
	v_or_b32_e32 v38, v214, v38
	v_or_b32_e32 v36, v40, v36
	v_min_f32_e32 v40, v39, v36
	v_max_f32_e32 v41, v37, v38
	v_min_f32_e32 v37, v37, v38
	v_max_f32_e32 v36, v39, v36
	v_max_f32_e32 v44, v42, v43
	v_max_f32_e32 v46, v45, v35
	v_min_f32_e32 v214, v41, v40
	v_min_f32_e32 v38, v37, v36
	v_min_f32_e32 v42, v42, v43
	v_min_f32_e32 v35, v45, v35
	v_max_f32_e32 v40, v41, v40
	v_max_f32_e32 v36, v37, v36
	v_max_f32_e32 v47, v44, v46
	v_min_f32_e32 v39, v214, v38
	v_max_f32_e32 v43, v42, v35
	v_min_f32_e32 v37, v40, v36
	v_min_f32_e32 v44, v44, v46
	v_max_f32_e32 v38, v214, v38
	v_min_f32_e32 v35, v42, v35
	v_max_f32_e32 v36, v40, v36
	v_min_f32_e32 v218, v221, v217
	v_max_f32_e32 v217, v221, v217
	v_min_f32_e32 v229, v47, v39
	v_min_f32_e32 v41, v43, v37
	v_min_f32_e32 v46, v44, v38
	v_min_f32_e32 v40, v35, v36
	v_max_f32_e32 v39, v47, v39
	v_max_f32_e32 v37, v43, v37
	v_max_f32_e32 v38, v44, v38
	v_max_f32_e32 v35, v35, v36
	v_max_f32_e32 v222, v220, v218
	v_max_f32_e32 v223, v215, v216
	v_max_f32_e32 v221, v219, v217
	v_max_f32_e32 v226, v54, v225
	v_min_f32_e32 v218, v220, v218
	v_min_f32_e32 v215, v215, v216
	v_min_f32_e32 v217, v219, v217
	v_min_f32_e32 v54, v54, v225
	v_min_f32_e32 v43, v39, v37
	v_min_f32_e32 v36, v38, v35
	v_max_f32_e32 v37, v39, v37
	v_max_f32_e32 v35, v38, v35
	v_max_f32_e32 v216, v218, v215
	v_max_f32_e32 v219, v217, v54
	v_min_f32_e32 v44, v43, v36
	v_min_f32_e32 v215, v218, v215
	v_min_f32_e32 v54, v217, v54
	v_min_f32_e32 v38, v37, v35
	v_max_f32_e32 v43, v43, v36
	v_max_f32_e32 v35, v37, v35
	v_and_b32_e32 v37, 0xffffff80, v15
	v_mov_b32_e32 v36, v33
	v_pk_add_f32 v[32:33], v[32:33], v[36:37] op_sel_hi:[0,1]
	v_mov_b32_e32 v37, 0xe0
	v_max_f32_e32 v217, v215, v54
	v_min_f32_e32 v54, v215, v54
	v_cmp_gt_i32_e64 s[76:77], 0, v33
	v_and_b32_e32 v33, 0xffffff00, v33
	s_nop 0
	v_cndmask_b32_e64 v36, 15, v249, s[76:77]
	v_cmp_gt_i32_e64 s[76:77], 0, v32
	v_and_b32_e32 v32, 0xffffff00, v32
	v_or_b32_e32 v33, v36, v33
	v_cndmask_b32_e64 v37, 31, v37, s[76:77]
	v_or_b32_e32 v32, v37, v32
	v_max_f32_e32 v36, v32, v33
	v_min_f32_e32 v32, v32, v33
	v_max_f32_e32 v37, v36, v36
	v_max_f32_e32 v33, v32, v32
	v_max_f32_e32 v37, 0xff61b1e6, v37
	v_max_f32_e32 v33, 0xff61b1e6, v33
	v_max_f32_e32 v224, v222, v223
	v_max_f32_e32 v233, v37, v33
	v_min_f32_e32 v33, v37, v33
	v_max_f32_e32 v234, 0xff61b1e6, v233
	v_max_f32_e32 v37, 0xff61b1e6, v33
	v_cmp_nlt_f32_e32 vcc, s28, v33
	v_max_f32_e32 v227, v221, v226
	v_max_f32_e32 v235, v234, v37
	v_cmp_nlt_f32_e64 s[88:89], s28, v235
	v_cndmask_b32_e32 v33, v199, v33, vcc
	v_min_f32_e32 v45, v229, v41
	v_cndmask_b32_e64 v236, v199, v235, s[88:89]
	v_cmp_nlt_f32_e64 s[88:89], s28, v233
	v_min_f32_e32 v42, v46, v40
	v_min_f32_e32 v222, v222, v223
	v_cndmask_b32_e64 v233, v199, v233, s[88:89]
	v_cmp_nlt_f32_e64 s[88:89], s28, v36
	v_min_f32_e32 v221, v221, v226
	v_max_f32_e32 v41, v229, v41
	v_cndmask_b32_e64 v36, v199, v36, s[88:89]
	v_cmp_nlt_f32_e64 s[88:89], s28, v32
	v_max_f32_e32 v40, v46, v40
	s_nop 0
	v_cndmask_b32_e64 v32, v199, v32, s[88:89]
	v_max_f32_e32 v237, v36, v32
	v_min_f32_e32 v32, v36, v32
	v_max_f32_e32 v238, v233, v237
	v_max_f32_e32 v36, v33, v32
	v_max_f32_e32 v228, v224, v227
	v_min_f32_e32 v214, v45, v42
	v_max_f32_e32 v220, v216, v219
	v_max_f32_e32 v223, v222, v221
	v_min_f32_e32 v46, v41, v40
	v_min_f32_e32 v224, v224, v227
	v_max_f32_e32 v42, v45, v42
	v_min_f32_e32 v216, v216, v219
	v_min_f32_e32 v221, v222, v221
	v_max_f32_e32 v40, v41, v40
	v_max_f32_e32 v239, v238, v36
	v_min_f32_e32 v233, v233, v237
	v_min_f32_e32 v32, v33, v32
	v_min_f32_e32 v37, v234, v37
	v_min_f32_e32 v36, v238, v36
	v_max_f32_e32 v52, v49, v52
	s_mov_b64 s[6:7], s[96:97]
	v_cmp_nlt_f32_e64 s[88:89], s28, v239
	v_cmp_nlt_f32_e64 s[76:77], s28, v37
	v_cmp_nlt_f32_e64 s[14:15], s28, v36
	v_max_f32_e32 v230, v228, v214
	v_max_f32_e32 v47, v220, v44
	v_max_f32_e32 v226, v223, v46
	v_max_f32_e32 v39, v217, v38
	v_max_f32_e32 v45, v224, v42
	v_max_f32_e32 v219, v216, v43
	v_max_f32_e32 v41, v221, v40
	v_max_f32_e32 v215, v54, v35
	v_cndmask_b32_e64 v240, v199, v239, s[88:89]
	v_max_f32_e32 v33, v233, v32
	v_cndmask_b32_e64 v234, v199, v37, s[76:77]
	v_cndmask_b32_e64 v238, v199, v36, s[14:15]
	v_min_f32_e32 v32, v233, v32
	v_cmp_nlt_f32_e64 s[88:89], s28, v33
	v_cmp_nlt_f32_e32 vcc, s28, v32
	v_max_f32_e32 v48, v243, v245
	v_max_f32_e32 v225, v230, v47
	v_max_f32_e32 v218, v226, v39
	v_max_f32_e32 v227, v45, v219
	v_max_f32_e32 v222, v41, v215
	v_min_f32_e32 v241, v236, v240
	v_cndmask_b32_e64 v237, v199, v33, s[88:89]
	v_min_f32_e32 v243, v234, v238
	v_cndmask_b32_e32 v233, v199, v32, vcc
	v_max_f32_e32 v229, v225, v218
	v_max_f32_e32 v231, v227, v222
	v_min_f32_e32 v242, v241, v237
	v_min_f32_e32 v244, v243, v233
	v_min_f32_e32 v214, v228, v214
	v_max_f32_e32 v232, v229, v231
	v_min_f32_e32 v245, v242, v244
	v_max_f32_e32 v228, 0xff61b1e6, v235
	v_max_f32_e32 v235, v239, v239
	v_max_f32_e32 v36, v36, v36
	v_min_f32_e32 v44, v220, v44
	v_min_f32_e32 v46, v223, v46
	v_min_f32_e32 v38, v217, v38
	v_min_f32_e32 v42, v224, v42
	v_min_f32_e32 v43, v216, v43
	v_min_f32_e32 v40, v221, v40
	v_min_f32_e32 v35, v54, v35
	v_max_f32_e32 v235, 0xff61b1e6, v235
	v_max_f32_e32 v33, v33, v33
	v_max_f32_e32 v37, 0xff61b1e6, v37
	v_max_f32_e32 v36, 0xff61b1e6, v36
	v_max_f32_e32 v32, v32, v32
	v_max_f32_e32 v232, v232, v245
	s_mov_b32 s36, s18
	v_max_f32_e32 v33, 0xff61b1e6, v33
	v_max_f32_e32 v32, 0xff61b1e6, v32
	v_max_f32_e32 v220, v214, v44
	v_max_f32_e32 v217, v46, v38
	v_max_f32_e32 v216, v42, v43
	v_max_f32_e32 v54, v40, v35
	v_min_f32_e32 v239, v228, v235
	v_min_f32_e32 v245, 0xff61b1e6, v33
	v_min_f32_e32 v247, v37, v36
	v_min_f32_e32 v248, 0xff61b1e6, v32
	v_max_f32_e32 v223, v220, v217
	v_max_f32_e32 v221, v216, v54
	v_min_f32_e32 v246, v239, v245
	v_min_f32_e32 v249, v247, v248
	v_min_f32_e32 v47, v230, v47
	v_max_f32_e32 v230, v236, v240
	v_cmp_ngt_f32_e64 s[16:17], s28, v237
	v_max_f32_e32 v234, v234, v238
	v_cmp_ngt_f32_e64 s[14:15], s28, v233
	v_min_f32_e32 v44, v214, v44
	v_min_f32_e32 v38, v46, v38
	v_min_f32_e32 v42, v42, v43
	v_min_f32_e32 v35, v40, v35
	v_max_f32_e32 v214, v228, v235
	v_max_f32_e32 v36, v37, v36
	v_max_f32_e32 v224, v223, v221
	v_min_f32_e32 v250, v246, v249
	v_min_f32_e32 v39, v226, v39
	v_min_f32_e32 v45, v45, v219
	v_min_f32_e32 v41, v41, v215
	v_cndmask_b32_e64 v236, v199, v237, s[16:17]
	v_cndmask_b32_e64 v238, v199, v233, s[14:15]
	v_max_f32_e32 v46, v44, v38
	v_max_f32_e32 v40, v42, v35
	v_min_f32_e32 v228, v214, v33
	v_min_f32_e32 v37, v36, v32
	v_max_f32_e32 v224, v224, v250
	v_max_f32_e32 v226, v47, v39
	v_max_f32_e32 v215, v45, v41
	v_min_f32_e32 v240, v230, v236
	v_min_f32_e32 v250, v234, v238
	v_min_f32_e32 v218, v225, v218
	v_min_f32_e32 v222, v227, v222
	v_max_f32_e32 v237, v241, v237
	v_max_f32_e32 v233, v243, v233
	v_min_f32_e32 v39, v47, v39
	v_min_f32_e32 v41, v45, v41
	v_max_f32_e32 v47, v230, v236
	v_max_f32_e32 v230, v234, v238
	v_max_f32_e32 v43, v46, v40
	v_min_f32_e32 v235, v228, v37
	v_min_f32_e32 v217, v220, v217
	v_min_f32_e32 v54, v216, v54
	v_max_f32_e32 v239, v239, v245
	v_max_f32_e32 v243, v247, v248
	v_min_f32_e32 v38, v44, v38
	v_min_f32_e32 v35, v42, v35
	v_max_f32_e32 v33, v214, v33
	v_max_f32_e32 v32, v36, v32
	v_max_f32_e32 v219, v226, v215
	v_max_f32_e32 v227, v218, v222
	v_min_f32_e32 v241, v237, v233
	v_max_f32_e32 v45, v39, v41
	v_min_f32_e32 v234, v47, v230
	v_min_f32_e32 v229, v229, v231
	v_max_f32_e32 v231, v242, v244
	v_min_f32_e32 v215, v226, v215
	v_max_f32_e32 v226, v240, v250
	v_min_f32_e32 v251, v240, v250
	v_max_f32_e32 v43, v43, v235
	v_max_f32_e32 v216, v217, v54
	v_min_f32_e32 v245, v239, v243
	v_max_f32_e32 v42, v38, v35
	v_min_f32_e32 v36, v33, v32
	v_min_f32_e32 v221, v223, v221
	v_max_f32_e32 v223, v246, v249
	v_min_f32_e32 v40, v46, v40
	v_max_f32_e32 v37, v228, v37
	v_min_f32_e32 v218, v218, v222
	v_max_f32_e32 v222, v237, v233
	v_min_f32_e32 v54, v217, v54
	v_max_f32_e32 v217, v239, v243
	v_min_f32_e32 v39, v39, v41
	v_max_f32_e32 v41, v47, v230
	v_min_f32_e32 v35, v38, v35
	v_max_f32_e32 v32, v33, v32
	v_max_f32_e32 v227, v227, v241
	v_max_f32_e32 v45, v45, v234
	v_max_f32_e32 v229, v229, v231
	v_max_f32_e32 v215, v215, v226
	v_max_f32_e32 v61, v48, v56
	v_max_f32_e32 v182, v34, v53
	v_max_f32_e32 v219, v219, v251
	v_max_f32_e32 v216, v216, v245
	v_max_f32_e32 v36, v42, v36
	v_max_f32_e32 v221, v221, v223
	v_max_f32_e32 v37, v40, v37
	v_max_f32_e32 v218, v218, v222
	v_max_f32_e32 v217, v54, v217
	v_max_f32_e32 v39, v39, v41
	v_max_f32_e32 v32, v35, v32
	v_max_f32_e32 v49, v50, v52
	v_max_f32_e32 v56, v55, v61
	v_max_f32_e32 v58, v63, v178
	v_max_f32_e32 v60, v180, v182
	v_max_f32_e32 v62, v183, v190
	v_max_f32_e32 v173, v195, v209
	v_max_f32_e32 v179, v210, v211
	v_max_f32_e32 v181, v212, v213
	v_min_f32_e32 v225, v232, v224
	v_min_f32_e32 v241, v219, v43
	v_min_f32_e32 v245, v227, v216
	v_min_f32_e32 v42, v45, v36
	v_min_f32_e32 v223, v229, v221
	v_min_f32_e32 v40, v215, v37
	v_min_f32_e32 v222, v218, v217
	v_min_f32_e32 v33, v39, v32
	v_max_f32_e32 v48, v49, v56
	v_max_f32_e32 v53, v58, v60
	v_max_f32_e32 v57, v62, v173
	v_max_f32_e32 v59, v179, v181
	v_min_f32_e32 v220, v225, v241
	v_min_f32_e32 v44, v245, v42
	v_min_f32_e32 v46, v223, v40
	v_min_f32_e32 v35, v222, v33
	v_max_f32_e32 v34, v48, v53
	v_max_f32_e32 v51, v57, v59
	v_min_f32_e32 v214, v220, v44
	v_min_f32_e32 v38, v46, v35
	v_min_f32_e32 v47, v55, v61
	v_max_f32_e32 v235, v34, v51
	v_min_f32_e32 v41, v214, v38
	v_min_f32_e32 v61, v63, v178
	v_min_f32_e32 v63, v180, v182
	v_max_f32_e32 v54, v235, v41
	v_min_f32_e32 v41, v50, v52
	v_min_f32_e32 v182, v183, v190
	v_min_f32_e32 v183, v195, v209
	v_min_f32_e32 v190, v210, v211
	v_min_f32_e32 v209, v212, v213
	v_max_f32_e32 v212, v232, v224
	v_max_f32_e32 v43, v219, v43
	v_max_f32_e32 v216, v227, v216
	v_max_f32_e32 v36, v45, v36
	v_max_f32_e32 v221, v229, v221
	v_max_f32_e32 v37, v215, v37
	v_max_f32_e32 v217, v218, v217
	v_max_f32_e32 v32, v39, v32
	v_min_f32_e32 v49, v49, v56
	v_min_f32_e32 v224, v58, v60
	v_min_f32_e32 v62, v62, v173
	v_min_f32_e32 v173, v179, v181
	v_max_f32_e32 v181, v225, v241
	v_max_f32_e32 v42, v245, v42
	v_max_f32_e32 v40, v223, v40
	v_max_f32_e32 v33, v222, v33
	v_max_f32_e32 v50, v41, v47
	v_max_f32_e32 v178, v61, v63
	v_max_f32_e32 v195, v182, v183
	v_min_f32_e32 v213, v212, v43
	v_min_f32_e32 v45, v216, v36
	v_min_f32_e32 v215, v221, v37
	v_min_f32_e32 v39, v217, v32
	v_max_f32_e32 v226, v49, v224
	v_max_f32_e32 v179, v62, v173
	v_min_f32_e32 v225, v181, v42
	v_min_f32_e32 v222, v40, v33
	v_min_f32_e32 v41, v41, v47
	v_min_f32_e32 v47, v61, v63
	v_min_f32_e32 v63, v182, v183
	v_min_f32_e32 v182, v190, v209
	v_max_f32_e32 v43, v212, v43
	v_max_f32_e32 v36, v216, v36
	v_max_f32_e32 v37, v221, v37
	v_max_f32_e32 v32, v217, v32
	v_cmp_gt_f32_e64 s[24:25], v63, v182
	v_max_f32_e32 v210, v190, v209
	v_max_f32_e32 v56, v226, v179
	v_min_f32_e32 v58, v225, v222
	v_max_f32_e32 v223, v41, v47
	v_cndmask_b32_e64 v183, v182, v63, s[24:25]
	v_min_f32_e32 v209, v43, v36
	v_min_f32_e32 v212, v37, v32
	v_max_f32_e32 v56, v56, v58
	v_max_f32_e32 v58, v223, v183
	v_min_f32_e32 v60, v209, v212
	v_min_f32_e32 v48, v48, v53
	v_min_f32_e32 v217, v57, v59
	v_max_f32_e32 v44, v220, v44
	v_max_f32_e32 v35, v46, v35
	v_max_f32_e32 v58, v58, v60
	v_max_f32_e32 v53, v48, v217
	v_min_f32_e32 v46, v44, v35
	v_max_f32_e32 v180, v50, v178
	v_min_f32_e32 v219, v213, v45
	v_min_f32_e32 v218, v215, v39
	v_max_f32_e32 v59, v53, v46
	v_min_f32_e32 v46, v50, v178
	v_min_f32_e32 v50, v195, v210
	v_max_f32_e32 v45, v213, v45
	v_max_f32_e32 v39, v215, v39
	v_min_f32_e32 v49, v49, v224
	v_max_f32_e32 v53, v46, v50
	v_min_f32_e32 v57, v45, v39
	v_min_f32_e32 v213, v62, v173
	v_max_f32_e32 v42, v181, v42
	v_max_f32_e32 v33, v40, v33
	v_max_f32_e32 v60, v53, v57
	v_cmp_gt_f32_e64 s[20:21], v49, v213
	v_max_f32_e32 v211, v195, v210
	s_nop 0
	v_cndmask_b32_e64 v57, v213, v49, s[20:21]
	v_min_f32_e32 v40, v42, v33
	v_max_f32_e32 v36, v43, v36
	v_max_f32_e32 v32, v37, v32
	v_max_f32_e32 v61, v57, v40
	v_min_f32_e32 v40, v41, v47
	v_cndmask_b32_e64 v41, v63, v182, s[24:25]
	v_cmp_gt_f32_e64 s[14:15], v40, v41
	v_min_f32_e32 v34, v34, v51
	s_nop 0
	v_cndmask_b32_e64 v47, v41, v40, s[14:15]
	v_min_f32_e32 v37, v36, v32
	s_mov_b64 s[96:97], s[6:7]
	v_max_f32_e32 v62, v47, v37
	v_max_f32_e32 v37, v214, v38
	v_max_f32_e32 v35, v44, v35
	v_min_f32_e32 v55, v219, v218
	v_max_f32_e32 v63, v34, v37
	v_min_f32_e32 v34, v180, v211
	v_max_f32_e32 v37, v219, v218
	v_max_f32_e32 v52, v180, v211
	v_max_f32_e32 v33, v42, v33
	v_max_f32_e32 v173, v34, v37
	v_min_f32_e32 v34, v226, v179
	v_max_f32_e32 v37, v225, v222
	v_max_f32_e32 v32, v36, v32
	v_max_f32_e32 v178, v34, v37
	v_min_f32_e32 v34, v223, v183
	v_max_f32_e32 v37, v209, v212
	v_max_f32_e32 v55, v52, v55
	v_max_f32_e32 v179, v34, v37
	v_min_f32_e32 v34, v48, v217
	v_max_f32_e32 v180, v34, v35
	v_min_f32_e32 v34, v46, v50
	v_max_f32_e32 v35, v45, v39
	v_max_f32_e32 v181, v34, v35
	v_cndmask_b32_e64 v34, v49, v213, s[20:21]
	v_max_f32_e32 v182, v34, v33
	v_cndmask_b32_e64 v33, v40, v41, s[14:15]
	v_min_f32_e32 v52, v54, v55
	v_min_f32_e32 v190, v56, v58
	v_max_f32_e32 v183, v33, v32
	v_min_f32_e32 v53, v59, v60
	v_min_f32_e32 v57, v61, v62
	v_min_f32_e32 v195, v63, v173
	v_min_f32_e32 v209, v178, v179
	v_min_f32_e32 v210, v180, v181
	v_min_f32_e32 v211, v182, v183
	v_min_f32_e32 v216, v52, v190
	v_min_f32_e32 v215, v53, v57
	v_min_f32_e32 v51, v195, v209
	v_min_f32_e32 v50, v210, v211
	s_movk_i32 s10, 0xff
	v_min_f32_e32 v220, v216, v215
	v_min_f32_e32 v212, v51, v50
	s_movk_i32 s8, 0x7f
	v_bitop3_b32 v35, v31, s8, v31 bitop3:0xc
	v_min_f32_e32 v32, v220, v212
	v_and_b32_e32 v33, 0xff, v32
	v_bitop3_b32 v34, v32, s10, v32 bitop3:0xc
	v_cmp_gt_i32_e64 s[6:7], 0, v32
	v_readlane_b32 s94, v255, 39
	v_readlane_b32 s95, v255, 40
	v_cndmask_b32_e64 v213, v34, v33, s[6:7]
	v_and_b32_e32 v33, 0x7f, v31
	v_cmp_gt_i32_e64 s[6:7], 0, v31
	v_and_b32_e32 v34, 15, v213
	v_lshrrev_b32_e32 v214, 4, v213
	v_cndmask_b32_e64 v31, v35, v33, s[6:7]
	v_and_b32_e32 v33, 0x7f, v30
	v_bitop3_b32 v35, v30, s8, v30 bitop3:0xc
	v_cmp_gt_i32_e64 s[6:7], 0, v30
	v_readlane_b32 s86, v255, 31
	v_readlane_b32 s82, v255, 33
	v_cndmask_b32_e64 v30, v35, v33, s[6:7]
	v_and_b32_e32 v33, 0x7f, v29
	v_bitop3_b32 v35, v29, s8, v29 bitop3:0xc
	v_cmp_gt_i32_e64 s[6:7], 0, v29
	v_readlane_b32 s84, v255, 25
	v_readlane_b32 s87, v255, 32
	v_cndmask_b32_e64 v29, v35, v33, s[6:7]
	v_and_b32_e32 v33, 0x7f, v28
	v_bitop3_b32 v35, v28, s8, v28 bitop3:0xc
	v_cmp_gt_i32_e64 s[6:7], 0, v28
	v_readlane_b32 s92, v255, 35
	v_readlane_b32 s88, v255, 29
	v_cndmask_b32_e64 v28, v35, v33, s[6:7]
	v_and_b32_e32 v33, 0x7f, v27
	v_bitop3_b32 v35, v27, s8, v27 bitop3:0xc
	v_cmp_gt_i32_e64 s[6:7], 0, v27
	v_readlane_b32 s90, v255, 27
	v_readlane_b32 s78, v255, 13
	v_cndmask_b32_e64 v27, v35, v33, s[6:7]
	v_and_b32_e32 v33, 0x7f, v26
	v_bitop3_b32 v35, v26, s8, v26 bitop3:0xc
	v_cmp_gt_i32_e64 s[6:7], 0, v26
	v_readlane_b32 s83, v255, 34
	v_readlane_b32 s74, v255, 9
	v_cndmask_b32_e64 v26, v35, v33, s[6:7]
	v_and_b32_e32 v33, 0x7f, v25
	v_bitop3_b32 v35, v25, s8, v25 bitop3:0xc
	v_cmp_gt_i32_e64 s[6:7], 0, v25
	v_readlane_b32 s85, v255, 26
	v_readlane_b32 s76, v255, 11
	v_cndmask_b32_e64 v25, v35, v33, s[6:7]
	v_and_b32_e32 v33, 0x7f, v24
	v_bitop3_b32 v35, v24, s8, v24 bitop3:0xc
	v_cmp_gt_i32_e64 s[6:7], 0, v24
	v_readlane_b32 s22, v255, 23
	v_readlane_b32 s34, v255, 17
	v_cndmask_b32_e64 v24, v35, v33, s[6:7]
	v_and_b32_e32 v33, 0x7f, v23
	v_bitop3_b32 v35, v23, s8, v23 bitop3:0xc
	v_cmp_gt_i32_e64 s[6:7], 0, v23
	v_readlane_b32 s30, v255, 15
	v_readlane_b32 s81, v255, 41
	v_cndmask_b32_e64 v23, v35, v33, s[6:7]
	v_and_b32_e32 v33, 0x7f, v22
	v_bitop3_b32 v35, v22, s8, v22 bitop3:0xc
	v_cmp_gt_i32_e64 s[6:7], 0, v22
	s_movk_i32 s87, 0x4000
	v_readlane_b32 s93, v255, 36
	v_cndmask_b32_e64 v22, v35, v33, s[6:7]
	v_and_b32_e32 v33, 0x7f, v21
	v_bitop3_b32 v35, v21, s8, v21 bitop3:0xc
	v_cmp_gt_i32_e64 s[6:7], 0, v21
	v_readlane_b32 s89, v255, 30
	v_readlane_b32 s91, v255, 28
	v_cndmask_b32_e64 v21, v35, v33, s[6:7]
	v_and_b32_e32 v33, 0x7f, v20
	v_bitop3_b32 v35, v20, s8, v20 bitop3:0xc
	v_cmp_gt_i32_e64 s[6:7], 0, v20
	v_readlane_b32 s79, v255, 14
	v_readlane_b32 s83, v255, 37
	v_cndmask_b32_e64 v20, v35, v33, s[6:7]
	v_and_b32_e32 v33, 0x7f, v19
	v_bitop3_b32 v35, v19, s8, v19 bitop3:0xc
	v_cmp_gt_i32_e64 s[6:7], 0, v19
	v_readlane_b32 s75, v255, 10
	v_readlane_b32 s85, v255, 38
	v_cndmask_b32_e64 v19, v35, v33, s[6:7]
	v_and_b32_e32 v33, 0x7f, v18
	v_bitop3_b32 v35, v18, s8, v18 bitop3:0xc
	v_cmp_gt_i32_e64 s[6:7], 0, v18
	v_readlane_b32 s77, v255, 12
	v_readlane_b32 s23, v255, 24
	v_cndmask_b32_e64 v18, v35, v33, s[6:7]
	v_and_b32_e32 v33, 0x7f, v17
	v_bitop3_b32 v35, v17, s8, v17 bitop3:0xc
	v_cmp_gt_i32_e64 s[6:7], 0, v17
	s_mov_b32 s18, s36
	s_movk_i32 s27, 0x1200
	v_cndmask_b32_e64 v17, v35, v33, s[6:7]
	v_and_b32_e32 v33, 0x7f, v16
	v_bitop3_b32 v35, v16, s8, v16 bitop3:0xc
	v_cmp_gt_i32_e64 s[6:7], 0, v16
	v_readlane_b32 s35, v255, 18
	v_readlane_b32 s31, v255, 16
	v_cndmask_b32_e64 v33, v35, v33, s[6:7]
	v_lshl_add_u32 v252, v34, 8, v207
	ds_read_b32 v16, v252 offset:4096
	v_bitop3_b32 v35, v15, s8, v15 bitop3:0xc
	s_nop 0
	s_nop 1
	s_nop 1
	s_nop 1
	s_nop 1
	s_nop 1
	s_nop 1
	s_nop 1
	s_nop 1
	s_nop 1
	s_nop 1
	s_nop 1
	s_nop 1
	s_nop 1
	s_nop 1
	v_and_b32_e32 v34, 0x7f, v15
	s_nop 0
	s_waitcnt lgkmcnt(0)
	v_and_b32_e32 v252, 0x7f, v16
	v_cmp_gt_i32_e64 s[6:7], 0, v16
	v_xor_b32_e32 v16, 0x7f, v252
	s_nop 0
	v_cndmask_b32_e64 v16, v16, v252, s[6:7]
	v_cmp_gt_i32_e64 s[6:7], 0, v15
	v_and_b32_e32 v15, 0x7f, v14
	s_nop 0
	v_cndmask_b32_e64 v34, v35, v34, s[6:7]
	v_bitop3_b32 v35, v14, s8, v14 bitop3:0xc
	v_cmp_gt_i32_e64 s[6:7], 0, v14
	v_and_b32_e32 v14, 0x7f, v13
	s_nop 0
	v_cndmask_b32_e64 v35, v35, v15, s[6:7]
	v_bitop3_b32 v15, v13, s8, v13 bitop3:0xc
	v_cmp_gt_i32_e64 s[6:7], 0, v13
	v_and_b32_e32 v13, 0x7f, v12
	s_nop 0
	v_cndmask_b32_e64 v36, v15, v14, s[6:7]
	v_bitop3_b32 v14, v12, s8, v12 bitop3:0xc
	v_cmp_gt_i32_e64 s[6:7], 0, v12
	v_and_b32_e32 v12, 0x7f, v11
	v_max_f32_e32 v15, v59, v60
	v_cndmask_b32_e64 v37, v14, v13, s[6:7]
	v_bitop3_b32 v13, v11, s8, v11 bitop3:0xc
	v_cmp_gt_i32_e64 s[6:7], 0, v11
	v_and_b32_e32 v11, 0x7f, v10
	v_max_f32_e32 v14, v56, v58
	v_cndmask_b32_e64 v38, v13, v12, s[6:7]
	v_bitop3_b32 v12, v10, s8, v10 bitop3:0xc
	v_cmp_gt_i32_e64 s[6:7], 0, v10
	v_and_b32_e32 v10, 0x7f, v9
	v_max_f32_e32 v59, v61, v62
	v_cndmask_b32_e64 v39, v12, v11, s[6:7]
	v_bitop3_b32 v11, v9, s8, v9 bitop3:0xc
	v_cmp_gt_i32_e64 s[6:7], 0, v9
	v_and_b32_e32 v9, 0x7f, v8
	v_max_f32_e32 v60, v63, v173
	v_cndmask_b32_e64 v40, v11, v10, s[6:7]
	v_bitop3_b32 v10, v8, s8, v8 bitop3:0xc
	v_cmp_gt_i32_e64 s[6:7], 0, v8
	v_and_b32_e32 v8, 0x7f, v7
	v_max_f32_e32 v61, v178, v179
	v_cndmask_b32_e64 v41, v10, v9, s[6:7]
	v_bitop3_b32 v9, v7, s8, v7 bitop3:0xc
	v_cmp_gt_i32_e64 s[6:7], 0, v7
	v_and_b32_e32 v7, 0x7f, v6
	v_max_f32_e32 v62, v180, v181
	v_cndmask_b32_e64 v42, v9, v8, s[6:7]
	v_bitop3_b32 v8, v6, s8, v6 bitop3:0xc
	v_cmp_gt_i32_e64 s[6:7], 0, v6
	v_and_b32_e32 v6, 0x7f, v5
	v_max_f32_e32 v9, v210, v211
	v_cndmask_b32_e64 v43, v8, v7, s[6:7]
	v_bitop3_b32 v7, v5, s8, v5 bitop3:0xc
	v_cmp_gt_i32_e64 s[6:7], 0, v5
	v_and_b32_e32 v5, 0x7f, v4
	v_max_f32_e32 v8, v195, v209
	v_cndmask_b32_e64 v44, v7, v6, s[6:7]
	v_bitop3_b32 v6, v4, s8, v4 bitop3:0xc
	v_cmp_gt_i32_e64 s[6:7], 0, v4
	v_and_b32_e32 v4, 0x7f, v3
	v_max_f32_e32 v63, v182, v183
	v_cndmask_b32_e64 v45, v6, v5, s[6:7]
	v_bitop3_b32 v5, v3, s8, v3 bitop3:0xc
	v_cmp_gt_i32_e64 s[6:7], 0, v3
	v_and_b32_e32 v3, 0x7f, v2
	s_nop 0
	v_cndmask_b32_e64 v46, v5, v4, s[6:7]
	v_bitop3_b32 v4, v2, s8, v2 bitop3:0xc
	v_cmp_gt_i32_e64 s[6:7], 0, v2
	v_and_b32_e32 v2, 0x7f, v1
	s_nop 0
	v_cndmask_b32_e64 v47, v4, v3, s[6:7]
	v_bitop3_b32 v3, v1, s8, v1 bitop3:0xc
	v_cmp_gt_i32_e64 s[6:7], 0, v1
	v_and_b32_e32 v1, 0x7f, v0
	v_max_f32_e32 v4, v51, v50
	v_cndmask_b32_e64 v48, v3, v2, s[6:7]
	v_bitop3_b32 v2, v0, s8, v0 bitop3:0xc
	v_cmp_gt_i32_e64 s[6:7], 0, v0
	v_min_f32_e32 v56, v60, v61
	s_nop 0
	v_cndmask_b32_e64 v49, v2, v1, s[6:7]
	v_lshl_add_u32 v252, v214, 8, v207
	ds_read_b32 v0, v252
	v_min_f32_e32 v58, v62, v63
	s_nop 0
	v_max_f32_e32 v60, v60, v61
	v_max_f32_e32 v61, v62, v63
	v_readlane_b32 s46, v255, 21
	v_readlane_b32 s44, v255, 19
	v_readlane_b32 s47, v255, 22
	v_readlane_b32 s45, v255, 20
	s_nop 1
	s_nop 1
	s_nop 1
	s_nop 1
	s_nop 1
	s_nop 1
	s_nop 1
	s_nop 1
	s_nop 1
	s_nop 1
	s_nop 1
	s_nop 1
	s_waitcnt lgkmcnt(0)
	v_and_b32_e32 v252, 0x7f, v0
	v_cmp_gt_i32_e64 s[6:7], 0, v0
	v_xor_b32_e32 v0, 0x7f, v252
	s_nop 0
	v_cndmask_b32_e64 v3, v0, v252, s[6:7]
	v_max_f32_e32 v0, v220, v212
	v_and_b32_e32 v1, 0xff, v0
	v_bitop3_b32 v2, v0, s10, v0 bitop3:0xc
	v_cmp_gt_i32_e64 s[6:7], 0, v0
	v_and_b32_e32 v12, 0xffffff00, v0
	v_lshl_add_u32 v3, v3, 7, v16
	v_cndmask_b32_e64 v0, v2, v1, s[6:7]
	v_lshrrev_b32_e32 v1, 4, v0
	v_lshl_add_u32 v252, v1, 8, v207
	ds_read_b32 v2, v252
	v_and_b32_e32 v0, 15, v0
	s_nop 0
	s_nop 1
	s_nop 1
	s_nop 1
	s_nop 1
	s_nop 1
	s_nop 1
	s_nop 1
	s_nop 1
	s_nop 1
	s_nop 1
	s_nop 1
	s_nop 1
	s_nop 1
	s_nop 1
	s_nop 1
	s_waitcnt lgkmcnt(0)
	v_and_b32_e32 v252, 0x7f, v2
	v_cmp_gt_i32_e64 s[6:7], 0, v2
	v_xor_b32_e32 v2, 0x7f, v252
	s_nop 0
	v_cndmask_b32_e64 v1, v2, v252, s[6:7]
	v_lshl_add_u32 v252, v0, 8, v207
	ds_read_b32 v2, v252 offset:4096
	s_nop 1
	s_nop 1
	s_nop 1
	s_nop 1
	s_nop 1
	s_nop 1
	s_nop 1
	s_nop 1
	s_nop 1
	s_nop 1
	s_nop 1
	s_nop 1
	s_nop 1
	s_nop 1
	s_nop 1
	s_nop 1
	s_waitcnt lgkmcnt(0)
	v_and_b32_e32 v252, 0x7f, v2
	v_cmp_gt_i32_e64 s[6:7], 0, v2
	v_xor_b32_e32 v2, 0x7f, v252
	s_nop 0
	v_cndmask_b32_e64 v0, v2, v252, s[6:7]
	v_lshl_add_u32 v2, v1, 7, v0
	v_max_f32_e32 v0, v216, v215
	v_min_f32_e32 v1, v0, v4
	v_and_b32_e32 v5, 0xff, v1
	v_bitop3_b32 v6, v1, s10, v1 bitop3:0xc
	v_cmp_gt_i32_e64 s[8:9], 0, v1
	v_and_b32_e32 v50, 0xffffff00, v1
	v_max_f32_e32 v0, v0, v4
	v_cndmask_b32_e64 v1, v6, v5, s[8:9]
	v_lshrrev_b32_e32 v5, 4, v1
	v_lshl_add_u32 v252, v5, 8, v207
	ds_read_b32 v6, v252
	v_and_b32_e32 v1, 15, v1
	v_and_b32_e32 v4, 0xff, v0
	v_cmp_gt_i32_e64 s[6:7], 0, v0
	v_and_b32_e32 v51, 0xffffff00, v0
	s_nop 1
	s_nop 1
	s_nop 1
	s_nop 1
	s_nop 1
	s_nop 1
	s_nop 1
	s_nop 1
	s_nop 1
	s_nop 1
	s_nop 1
	s_nop 1
	s_nop 1
	s_nop 1
	s_waitcnt lgkmcnt(0)
	v_and_b32_e32 v252, 0x7f, v6
	v_cmp_gt_i32_e64 s[8:9], 0, v6
	v_xor_b32_e32 v6, 0x7f, v252
	s_nop 0
	v_cndmask_b32_e64 v5, v6, v252, s[8:9]
	v_lshl_add_u32 v252, v1, 8, v207
	ds_read_b32 v6, v252 offset:4096
	s_nop 1
	s_nop 1
	s_nop 1
	s_nop 1
	s_nop 1
	s_nop 1
	s_nop 1
	s_nop 1
	s_nop 1
	s_nop 1
	s_nop 1
	s_nop 1
	s_nop 1
	s_nop 1
	s_nop 1
	s_nop 1
	s_waitcnt lgkmcnt(0)
	v_and_b32_e32 v252, 0x7f, v6
	v_cmp_gt_i32_e64 s[8:9], 0, v6
	v_xor_b32_e32 v6, 0x7f, v252
	s_nop 0
	v_cndmask_b32_e64 v1, v6, v252, s[8:9]
	v_lshl_add_u32 v1, v5, 7, v1
	v_bitop3_b32 v5, v0, s10, v0 bitop3:0xc
	v_cndmask_b32_e64 v0, v5, v4, s[6:7]
	v_lshrrev_b32_e32 v4, 4, v0
	v_lshl_add_u32 v252, v4, 8, v207
	ds_read_b32 v5, v252
	v_and_b32_e32 v0, 15, v0
	s_nop 0
	s_nop 1
	s_nop 1
	s_nop 1
	s_nop 1
	s_nop 1
	s_nop 1
	s_nop 1
	s_nop 1
	s_nop 1
	s_nop 1
	s_nop 1
	s_nop 1
	s_nop 1
	s_nop 1
	s_nop 1
	s_waitcnt lgkmcnt(0)
	v_and_b32_e32 v252, 0x7f, v5
	v_cmp_gt_i32_e64 s[6:7], 0, v5
	v_xor_b32_e32 v5, 0x7f, v252
	s_nop 0
	v_cndmask_b32_e64 v4, v5, v252, s[6:7]
	v_lshl_add_u32 v252, v0, 8, v207
	ds_read_b32 v5, v252 offset:4096
	s_nop 1
	s_nop 1
	s_nop 1
	s_nop 1
	s_nop 1
	s_nop 1
	s_nop 1
	s_nop 1
	s_nop 1
	s_nop 1
	s_nop 1
	s_nop 1
	s_nop 1
	s_nop 1
	s_nop 1
	s_nop 1
	s_waitcnt lgkmcnt(0)
	v_and_b32_e32 v252, 0x7f, v5
	v_cmp_gt_i32_e64 s[6:7], 0, v5
	v_xor_b32_e32 v5, 0x7f, v252
	s_nop 0
	v_cndmask_b32_e64 v0, v5, v252, s[6:7]
	v_lshl_add_u32 v0, v4, 7, v0
	v_max_f32_e32 v4, v52, v190
	v_max_f32_e32 v5, v53, v57
	v_min_f32_e32 v6, v4, v5
	v_min_f32_e32 v10, v8, v9
	v_max_f32_e32 v4, v4, v5
	v_max_f32_e32 v8, v8, v9
	v_min_f32_e32 v7, v6, v10
	v_and_b32_e32 v11, 0xff, v7
	v_bitop3_b32 v13, v7, s10, v7 bitop3:0xc
	v_cmp_gt_i32_e64 s[8:9], 0, v7
	v_and_b32_e32 v52, 0xffffff00, v7
	v_max_f32_e32 v6, v6, v10
	v_cndmask_b32_e64 v7, v13, v11, s[8:9]
	v_lshrrev_b32_e32 v11, 4, v7
	v_lshl_add_u32 v252, v11, 8, v207
	ds_read_b32 v13, v252
	v_and_b32_e32 v7, 15, v7
	v_and_b32_e32 v10, 0xff, v6
	v_cmp_gt_i32_e64 s[6:7], 0, v6
	v_and_b32_e32 v53, 0xffffff00, v6
	s_nop 1
	s_nop 1
	s_nop 1
	s_nop 1
	s_nop 1
	s_nop 1
	s_nop 1
	s_nop 1
	s_nop 1
	s_nop 1
	s_nop 1
	s_nop 1
	s_nop 1
	s_nop 1
	s_waitcnt lgkmcnt(0)
	v_and_b32_e32 v252, 0x7f, v13
	v_cmp_gt_i32_e64 s[8:9], 0, v13
	v_xor_b32_e32 v13, 0x7f, v252
	s_nop 0
	v_cndmask_b32_e64 v11, v13, v252, s[8:9]
	v_lshl_add_u32 v252, v7, 8, v207
	ds_read_b32 v13, v252 offset:4096
	s_nop 1
	s_nop 1
	s_nop 1
	s_nop 1
	s_nop 1
	s_nop 1
	s_nop 1
	s_nop 1
	s_nop 1
	s_nop 1
	s_nop 1
	s_nop 1
	s_nop 1
	s_nop 1
	s_nop 1
	s_nop 1
	s_waitcnt lgkmcnt(0)
	v_and_b32_e32 v252, 0x7f, v13
	v_cmp_gt_i32_e64 s[8:9], 0, v13
	v_xor_b32_e32 v13, 0x7f, v252
	s_nop 0
	v_cndmask_b32_e64 v7, v13, v252, s[8:9]
	v_lshl_add_u32 v7, v11, 7, v7
	v_bitop3_b32 v11, v6, s10, v6 bitop3:0xc
	v_cndmask_b32_e64 v6, v11, v10, s[6:7]
	v_lshrrev_b32_e32 v10, 4, v6
	v_lshl_add_u32 v252, v10, 8, v207
	ds_read_b32 v11, v252
	v_and_b32_e32 v6, 15, v6
	v_max_f32_e32 v13, v54, v55
	v_min_f32_e32 v55, v56, v58
	s_nop 0
	v_max_f32_e32 v58, v56, v58
	s_nop 0
	s_nop 1
	s_nop 1
	s_nop 1
	s_nop 1
	s_nop 1
	s_nop 1
	s_nop 1
	s_nop 1
	s_nop 1
	s_nop 1
	s_nop 1
	s_nop 1
	s_nop 1
	s_waitcnt lgkmcnt(0)
	v_and_b32_e32 v252, 0x7f, v11
	v_cmp_gt_i32_e64 s[6:7], 0, v11
	v_xor_b32_e32 v11, 0x7f, v252
	s_nop 0
	v_cndmask_b32_e64 v10, v11, v252, s[6:7]
	v_lshl_add_u32 v252, v6, 8, v207
	ds_read_b32 v11, v252 offset:4096
	s_nop 1
	s_nop 1
	s_nop 1
	s_nop 1
	s_nop 1
	s_nop 1
	s_nop 1
	s_nop 1
	s_nop 1
	s_nop 1
	s_nop 1
	s_nop 1
	s_nop 1
	s_nop 1
	s_nop 1
	s_nop 1
	s_waitcnt lgkmcnt(0)
	v_and_b32_e32 v252, 0x7f, v11
	v_cmp_gt_i32_e64 s[6:7], 0, v11
	v_xor_b32_e32 v11, 0x7f, v252
	s_nop 0
	v_cndmask_b32_e64 v6, v11, v252, s[6:7]
	v_lshl_add_u32 v6, v10, 7, v6
	v_min_f32_e32 v5, v4, v8
	v_and_b32_e32 v9, 0xff, v5
	v_bitop3_b32 v10, v5, s10, v5 bitop3:0xc
	v_cmp_gt_i32_e64 s[8:9], 0, v5
	v_and_b32_e32 v57, 0xffffff00, v5
	v_max_f32_e32 v4, v4, v8
	v_cndmask_b32_e64 v5, v10, v9, s[8:9]
	v_lshrrev_b32_e32 v9, 4, v5
	v_lshl_add_u32 v252, v9, 8, v207
	ds_read_b32 v10, v252
	v_and_b32_e32 v5, 15, v5
	v_and_b32_e32 v8, 0xff, v4
	v_cmp_gt_i32_e64 s[6:7], 0, v4
	v_and_b32_e32 v209, 0xffffff00, v4
	s_nop 1
	s_nop 1
	s_nop 1
	s_nop 1
	s_nop 1
	s_nop 1
	s_nop 1
	s_nop 1
	s_nop 1
	s_nop 1
	s_nop 1
	s_nop 1
	s_nop 1
	s_nop 1
	s_waitcnt lgkmcnt(0)
	v_and_b32_e32 v252, 0x7f, v10
	v_cmp_gt_i32_e64 s[8:9], 0, v10
	v_xor_b32_e32 v10, 0x7f, v252
	s_nop 0
	v_cndmask_b32_e64 v9, v10, v252, s[8:9]
	v_lshl_add_u32 v252, v5, 8, v207
	ds_read_b32 v10, v252 offset:4096
	s_nop 1
	s_nop 1
	s_nop 1
	s_nop 1
	s_nop 1
	s_nop 1
	s_nop 1
	s_nop 1
	s_nop 1
	s_nop 1
	s_nop 1
	s_nop 1
	s_nop 1
	s_nop 1
	s_nop 1
	s_nop 1
	s_waitcnt lgkmcnt(0)
	v_and_b32_e32 v252, 0x7f, v10
	v_cmp_gt_i32_e64 s[8:9], 0, v10
	v_xor_b32_e32 v10, 0x7f, v252
	s_nop 0
	v_cndmask_b32_e64 v5, v10, v252, s[8:9]
	v_lshl_add_u32 v5, v9, 7, v5
	v_bitop3_b32 v9, v4, s10, v4 bitop3:0xc
	v_cndmask_b32_e64 v4, v9, v8, s[6:7]
	v_lshrrev_b32_e32 v8, 4, v4
	v_lshl_add_u32 v252, v8, 8, v207
	ds_read_b32 v9, v252
	v_and_b32_e32 v4, 15, v4
	s_nop 0
	s_nop 1
	s_nop 1
	s_nop 1
	s_nop 1
	s_nop 1
	s_nop 1
	s_nop 1
	s_nop 1
	s_nop 1
	s_nop 1
	s_nop 1
	s_nop 1
	s_nop 1
	s_nop 1
	s_nop 1
	s_waitcnt lgkmcnt(0)
	v_and_b32_e32 v252, 0x7f, v9
	v_cmp_gt_i32_e64 s[6:7], 0, v9
	v_xor_b32_e32 v9, 0x7f, v252
	s_nop 0
	v_cndmask_b32_e64 v8, v9, v252, s[6:7]
	v_lshl_add_u32 v252, v4, 8, v207
	ds_read_b32 v9, v252 offset:4096
	s_nop 1
	s_nop 1
	s_nop 1
	s_nop 1
	s_nop 1
	s_nop 1
	s_nop 1
	s_nop 1
	s_nop 1
	s_nop 1
	s_nop 1
	s_nop 1
	s_nop 1
	s_nop 1
	s_nop 1
	s_nop 1
	s_waitcnt lgkmcnt(0)
	v_and_b32_e32 v252, 0x7f, v9
	v_cmp_gt_i32_e64 s[6:7], 0, v9
	v_xor_b32_e32 v9, 0x7f, v252
	s_nop 0
	v_cndmask_b32_e64 v4, v9, v252, s[6:7]
	v_lshl_add_u32 v4, v8, 7, v4
	v_min_f32_e32 v8, v13, v14
	v_min_f32_e32 v9, v15, v59
	v_max_f32_e32 v13, v13, v14
	v_max_f32_e32 v59, v15, v59
	v_min_f32_e32 v10, v8, v9
	v_max_f32_e32 v8, v8, v9
	v_min_f32_e32 v11, v10, v55
	v_and_b32_e32 v173, 0xff, v11
	v_bitop3_b32 v178, v11, s10, v11 bitop3:0xc
	v_cmp_gt_i32_e64 s[8:9], 0, v11
	v_and_b32_e32 v54, 0xffffff00, v11
	v_max_f32_e32 v10, v10, v55
	v_cndmask_b32_e64 v11, v178, v173, s[8:9]
	v_lshrrev_b32_e32 v173, 4, v11
	v_lshl_add_u32 v252, v173, 8, v207
	ds_read_b32 v178, v252
	v_and_b32_e32 v11, 15, v11
	v_cmp_gt_i32_e64 s[6:7], 0, v10
	v_and_b32_e32 v55, 0xffffff00, v10
	s_nop 0
	v_min_f32_e32 v14, v13, v59
	v_min_f32_e32 v62, v60, v61
	v_max_f32_e32 v59, v13, v59
	v_max_f32_e32 v60, v60, v61
	s_nop 0
	s_nop 0
	v_min_f32_e32 v13, v59, v60
	v_and_b32_e32 v61, 0xffffff00, v13
	v_max_f32_e32 v59, v59, v60
	v_cmp_gt_i32_e32 vcc, 0, v59
	v_and_b32_e32 v60, 0xffffff00, v59
	v_sub_f32_e32 v12, v12, v60
	v_mul_f32_e32 v12, 0x3fb8aa3b, v12
	s_nop 0
	s_nop 1
	s_nop 1
	s_nop 1
	s_nop 1
	s_nop 1
	s_nop 1
	s_nop 1
	s_waitcnt lgkmcnt(0)
	v_and_b32_e32 v252, 0x7f, v178
	v_cmp_gt_i32_e64 s[8:9], 0, v178
	v_xor_b32_e32 v178, 0x7f, v252
	s_nop 0
	v_cndmask_b32_e64 v173, v178, v252, s[8:9]
	v_lshl_add_u32 v252, v11, 8, v207
	ds_read_b32 v178, v252 offset:4096
	s_nop 1
	s_nop 1
	s_nop 1
	s_nop 1
	s_nop 1
	s_nop 1
	s_nop 1
	s_nop 1
	s_nop 1
	s_nop 1
	s_nop 1
	s_nop 1
	s_nop 1
	s_nop 1
	s_nop 1
	s_nop 1
	s_waitcnt lgkmcnt(0)
	v_and_b32_e32 v252, 0x7f, v178
	v_cmp_gt_i32_e64 s[8:9], 0, v178
	v_xor_b32_e32 v178, 0x7f, v252
	s_nop 0
	v_cndmask_b32_e64 v11, v178, v252, s[8:9]
	v_lshl_add_u32 v11, v173, 7, v11
	v_and_b32_e32 v173, 0xff, v10
	v_bitop3_b32 v178, v10, s10, v10 bitop3:0xc
	v_cndmask_b32_e64 v10, v178, v173, s[6:7]
	v_lshrrev_b32_e32 v173, 4, v10
	v_lshl_add_u32 v252, v173, 8, v207
	ds_read_b32 v178, v252
	v_and_b32_e32 v10, 15, v10
	s_nop 0
	s_nop 1
	s_nop 1
	s_nop 1
	s_nop 1
	s_nop 1
	s_nop 1
	s_nop 1
	s_nop 1
	s_nop 1
	s_nop 1
	s_nop 1
	s_nop 1
	s_nop 1
	s_nop 1
	s_nop 1
	s_waitcnt lgkmcnt(0)
	v_and_b32_e32 v252, 0x7f, v178
	v_cmp_gt_i32_e64 s[6:7], 0, v178
	v_xor_b32_e32 v178, 0x7f, v252
	s_nop 0
	v_cndmask_b32_e64 v173, v178, v252, s[6:7]
	v_lshl_add_u32 v252, v10, 8, v207
	ds_read_b32 v178, v252 offset:4096
	s_nop 1
	s_nop 1
	s_nop 1
	s_nop 1
	s_nop 1
	s_nop 1
	s_nop 1
	s_nop 1
	s_nop 1
	s_nop 1
	s_nop 1
	s_nop 1
	s_nop 1
	s_nop 1
	s_nop 1
	s_nop 1
	s_waitcnt lgkmcnt(0)
	v_and_b32_e32 v252, 0x7f, v178
	v_cmp_gt_i32_e64 s[6:7], 0, v178
	v_xor_b32_e32 v178, 0x7f, v252
	s_nop 0
	v_cndmask_b32_e64 v10, v178, v252, s[6:7]
	v_lshl_add_u32 v10, v173, 7, v10
	v_min_f32_e32 v9, v8, v58
	v_and_b32_e32 v173, 0xff, v9
	v_bitop3_b32 v178, v9, s10, v9 bitop3:0xc
	v_cmp_gt_i32_e64 s[8:9], 0, v9
	v_and_b32_e32 v56, 0xffffff00, v9
	v_max_f32_e32 v8, v8, v58
	v_cndmask_b32_e64 v9, v178, v173, s[8:9]
	v_lshrrev_b32_e32 v173, 4, v9
	v_lshl_add_u32 v252, v173, 8, v207
	ds_read_b32 v178, v252
	v_and_b32_e32 v9, 15, v9
	v_cmp_gt_i32_e64 s[6:7], 0, v8
	v_and_b32_e32 v58, 0xffffff00, v8
	s_nop 0
	s_nop 1
	s_nop 1
	s_nop 1
	s_nop 1
	s_nop 1
	s_nop 1
	s_nop 1
	s_nop 1
	s_nop 1
	s_nop 1
	s_nop 1
	s_nop 1
	s_nop 1
	s_nop 1
	s_waitcnt lgkmcnt(0)
	v_and_b32_e32 v252, 0x7f, v178
	v_cmp_gt_i32_e64 s[8:9], 0, v178
	v_xor_b32_e32 v178, 0x7f, v252
	s_nop 0
	v_cndmask_b32_e64 v173, v178, v252, s[8:9]
	v_lshl_add_u32 v252, v9, 8, v207
	ds_read_b32 v178, v252 offset:4096
	s_nop 1
	s_nop 1
	s_nop 1
	s_nop 1
	s_nop 1
	s_nop 1
	s_nop 1
	s_nop 1
	s_nop 1
	s_nop 1
	s_nop 1
	s_nop 1
	s_nop 1
	s_nop 1
	s_nop 1
	s_nop 1
	s_waitcnt lgkmcnt(0)
	v_and_b32_e32 v252, 0x7f, v178
	v_cmp_gt_i32_e64 s[8:9], 0, v178
	v_xor_b32_e32 v178, 0x7f, v252
	s_nop 0
	v_cndmask_b32_e64 v9, v178, v252, s[8:9]
	v_lshl_add_u32 v9, v173, 7, v9
	v_and_b32_e32 v173, 0xff, v8
	v_bitop3_b32 v178, v8, s10, v8 bitop3:0xc
	v_cndmask_b32_e64 v8, v178, v173, s[6:7]
	v_lshrrev_b32_e32 v173, 4, v8
	v_lshl_add_u32 v252, v173, 8, v207
	ds_read_b32 v178, v252
	v_and_b32_e32 v8, 15, v8
	s_nop 0
	s_nop 1
	s_nop 1
	s_nop 1
	s_nop 1
	s_nop 1
	s_nop 1
	s_nop 1
	s_nop 1
	s_nop 1
	s_nop 1
	s_nop 1
	s_nop 1
	s_nop 1
	s_nop 1
	s_nop 1
	s_waitcnt lgkmcnt(0)
	v_and_b32_e32 v252, 0x7f, v178
	v_cmp_gt_i32_e64 s[6:7], 0, v178
	v_xor_b32_e32 v178, 0x7f, v252
	s_nop 0
	v_cndmask_b32_e64 v173, v178, v252, s[6:7]
	v_lshl_add_u32 v252, v8, 8, v207
	ds_read_b32 v178, v252 offset:4096
	s_nop 1
	s_nop 1
	s_nop 1
	s_nop 1
	s_nop 1
	s_nop 1
	s_nop 1
	s_nop 1
	s_nop 1
	s_nop 1
	s_nop 1
	s_nop 1
	s_nop 1
	s_nop 1
	s_nop 1
	s_nop 1
	s_waitcnt lgkmcnt(0)
	v_and_b32_e32 v252, 0x7f, v178
	v_cmp_gt_i32_e64 s[6:7], 0, v178
	v_xor_b32_e32 v178, 0x7f, v252
	s_nop 0
	v_cndmask_b32_e64 v8, v178, v252, s[6:7]
	v_lshl_add_u32 v8, v173, 7, v8
	v_min_f32_e32 v15, v14, v62
	v_and_b32_e32 v173, 0xff, v15
	v_bitop3_b32 v178, v15, s10, v15 bitop3:0xc
	v_cmp_gt_i32_e64 s[8:9], 0, v15
	v_and_b32_e32 v63, 0xffffff00, v15
	v_max_f32_e32 v14, v14, v62
	v_cndmask_b32_e64 v15, v178, v173, s[8:9]
	v_lshrrev_b32_e32 v173, 4, v15
	v_lshl_add_u32 v252, v173, 8, v207
	ds_read_b32 v178, v252
	v_and_b32_e32 v15, 15, v15
	v_cmp_gt_i32_e64 s[6:7], 0, v14
	v_and_b32_e32 v62, 0xffffff00, v14
	s_nop 0
	s_nop 1
	s_nop 1
	s_nop 1
	s_nop 1
	s_nop 1
	s_nop 1
	s_nop 1
	s_nop 1
	s_nop 1
	s_nop 1
	s_nop 1
	s_nop 1
	s_nop 1
	s_nop 1
	s_waitcnt lgkmcnt(0)
	v_and_b32_e32 v252, 0x7f, v178
	v_cmp_gt_i32_e64 s[8:9], 0, v178
	v_xor_b32_e32 v178, 0x7f, v252
	s_nop 0
	v_cndmask_b32_e64 v173, v178, v252, s[8:9]
	v_lshl_add_u32 v252, v15, 8, v207
	ds_read_b32 v178, v252 offset:4096
	s_nop 1
	s_nop 1
	s_nop 1
	s_nop 1
	s_nop 1
	s_nop 1
	s_nop 1
	s_nop 1
	s_nop 1
	s_nop 1
	s_nop 1
	s_nop 1
	s_nop 1
	s_nop 1
	s_nop 1
	s_nop 1
	s_waitcnt lgkmcnt(0)
	v_and_b32_e32 v252, 0x7f, v178
	v_cmp_gt_i32_e64 s[8:9], 0, v178
	v_xor_b32_e32 v178, 0x7f, v252
	s_nop 0
	v_cndmask_b32_e64 v15, v178, v252, s[8:9]
	v_lshl_add_u32 v15, v173, 7, v15
	v_and_b32_e32 v173, 0xff, v14
	v_bitop3_b32 v178, v14, s10, v14 bitop3:0xc
	v_cndmask_b32_e64 v14, v178, v173, s[6:7]
	v_lshrrev_b32_e32 v173, 4, v14
	v_lshl_add_u32 v252, v173, 8, v207
	ds_read_b32 v178, v252
	v_and_b32_e32 v14, 15, v14
	v_readlane_b32 s8, v253, 23
	v_readlane_b32 s9, v253, 24
	s_nop 0
	s_nop 1
	s_nop 1
	s_nop 1
	s_nop 1
	s_nop 1
	s_nop 1
	s_nop 1
	s_nop 1
	s_nop 1
	s_nop 1
	s_nop 1
	s_nop 1
	s_nop 1
	s_nop 1
	s_waitcnt lgkmcnt(0)
	v_and_b32_e32 v252, 0x7f, v178
	v_cmp_gt_i32_e64 s[6:7], 0, v178
	v_xor_b32_e32 v178, 0x7f, v252
	s_nop 0
	v_cndmask_b32_e64 v173, v178, v252, s[6:7]
	v_lshl_add_u32 v252, v14, 8, v207
	ds_read_b32 v178, v252 offset:4096
	s_nop 1
	s_nop 1
	s_nop 1
	s_nop 1
	s_nop 1
	s_nop 1
	s_nop 1
	s_nop 1
	s_nop 1
	s_nop 1
	s_nop 1
	s_nop 1
	s_nop 1
	s_nop 1
	s_nop 1
	s_nop 1
	s_waitcnt lgkmcnt(0)
	v_and_b32_e32 v252, 0x7f, v178
	v_cmp_gt_i32_e64 s[6:7], 0, v178
	v_xor_b32_e32 v178, 0x7f, v252
	s_nop 0
	v_cndmask_b32_e64 v14, v178, v252, s[6:7]
	v_lshl_add_u32 v14, v173, 7, v14
	v_and_b32_e32 v173, 0xff, v13
	v_bitop3_b32 v178, v13, s10, v13 bitop3:0xc
	v_cmp_gt_i32_e64 s[6:7], 0, v13
	s_nop 1
	v_cndmask_b32_e64 v13, v178, v173, s[6:7]
	v_lshrrev_b32_e32 v173, 4, v13
	v_lshl_add_u32 v252, v173, 8, v207
	ds_read_b32 v178, v252
	v_and_b32_e32 v13, 15, v13
	s_nop 0
	s_nop 1
	s_nop 1
	s_nop 1
	s_nop 1
	s_nop 1
	s_nop 1
	s_nop 1
	s_nop 1
	s_nop 1
	s_nop 1
	s_nop 1
	s_nop 1
	s_nop 1
	s_nop 1
	s_nop 1
	s_waitcnt lgkmcnt(0)
	v_and_b32_e32 v252, 0x7f, v178
	v_cmp_gt_i32_e64 s[6:7], 0, v178
	v_xor_b32_e32 v178, 0x7f, v252
	s_nop 0
	v_cndmask_b32_e64 v173, v178, v252, s[6:7]
	v_lshl_add_u32 v252, v13, 8, v207
	ds_read_b32 v178, v252 offset:4096
	s_nop 1
	s_nop 1
	s_nop 1
	s_nop 1
	s_nop 1
	s_nop 1
	s_nop 1
	s_nop 1
	s_nop 1
	s_nop 1
	s_nop 1
	s_nop 1
	s_nop 1
	s_nop 1
	s_nop 1
	s_nop 1
	s_waitcnt lgkmcnt(0)
	v_and_b32_e32 v252, 0x7f, v178
	v_cmp_gt_i32_e64 s[6:7], 0, v178
	v_xor_b32_e32 v178, 0x7f, v252
	s_nop 0
	v_cndmask_b32_e64 v13, v178, v252, s[6:7]
	v_lshl_add_u32 v13, v173, 7, v13
	v_and_b32_e32 v173, 0xff, v59
	v_bitop3_b32 v178, v59, s10, v59 bitop3:0xc
	v_cndmask_b32_e32 v59, v178, v173, vcc
	v_lshrrev_b32_e32 v173, 4, v59
	v_cmp_gt_u32_e32 vcc, 16, v59
	s_nop 1
	v_cndmask_b32_e32 v49, 0, v49, vcc
	v_cmp_eq_u32_e32 vcc, 1, v173
	s_nop 1
	v_cndmask_b32_e32 v48, v49, v48, vcc
	v_cmp_eq_u32_e32 vcc, 2, v173
	s_nop 1
	v_cndmask_b32_e32 v47, v48, v47, vcc
	v_cmp_eq_u32_e32 vcc, 3, v173
	s_nop 1
	v_cndmask_b32_e32 v46, v47, v46, vcc
	v_cmp_eq_u32_e32 vcc, 4, v173
	s_nop 1
	v_cndmask_b32_e32 v45, v46, v45, vcc
	v_cmp_eq_u32_e32 vcc, 5, v173
	s_nop 1
	v_cndmask_b32_e32 v44, v45, v44, vcc
	v_cmp_eq_u32_e32 vcc, 6, v173
	s_nop 1
	v_cndmask_b32_e32 v43, v44, v43, vcc
	v_cmp_eq_u32_e32 vcc, 7, v173
	s_nop 1
	v_cndmask_b32_e32 v42, v43, v42, vcc
	v_cmp_eq_u32_e32 vcc, 8, v173
	s_nop 1
	v_cndmask_b32_e32 v41, v42, v41, vcc
	v_cmp_eq_u32_e32 vcc, 9, v173
	s_nop 1
	v_cndmask_b32_e32 v40, v41, v40, vcc
	v_cmp_eq_u32_e32 vcc, 10, v173
	s_nop 1
	v_cndmask_b32_e32 v39, v40, v39, vcc
	v_cmp_eq_u32_e32 vcc, 11, v173
	s_nop 1
	v_cndmask_b32_e32 v38, v39, v38, vcc
	v_cmp_eq_u32_e32 vcc, 12, v173
	v_and_b32_e32 v39, 15, v59
	s_nop 0
	v_cndmask_b32_e32 v37, v38, v37, vcc
	v_cmp_eq_u32_e32 vcc, 13, v173
	s_nop 1
	v_cndmask_b32_e32 v36, v37, v36, vcc
	v_cmp_eq_u32_e32 vcc, 14, v173
	s_nop 1
	v_cndmask_b32_e32 v35, v36, v35, vcc
	v_cmp_eq_u32_e32 vcc, 15, v173
	v_exp_f32_e32 v36, v12
	v_and_b32_e32 v12, 0xffffff00, v32
	v_cndmask_b32_e32 v38, v35, v34, vcc
	v_cmp_eq_u32_e32 vcc, 0, v39
	v_sub_f32_e32 v12, v12, v60
	v_mul_f32_e32 v12, 0x3fb8aa3b, v12
	v_cndmask_b32_e32 v33, 0, v33, vcc
	v_cmp_eq_u32_e32 vcc, 1, v39
	v_exp_f32_e32 v37, v12
	s_nop 0
	v_cndmask_b32_e32 v17, v33, v17, vcc
	v_cmp_eq_u32_e32 vcc, 2, v39
	v_sub_f32_e32 v33, v51, v60
	v_mul_f32_e32 v33, 0x3fb8aa3b, v33
	v_cndmask_b32_e32 v17, v17, v18, vcc
	v_cmp_eq_u32_e32 vcc, 3, v39
	v_sub_f32_e32 v18, v60, v60
	v_mul_f32_e32 v18, 0x3fb8aa3b, v18
	v_cndmask_b32_e32 v17, v17, v19, vcc
	v_cmp_eq_u32_e32 vcc, 4, v39
	v_sub_f32_e32 v19, v61, v60
	v_exp_f32_e32 v18, v18
	v_cndmask_b32_e32 v17, v17, v20, vcc
	v_cmp_eq_u32_e32 vcc, 5, v39
	v_mul_f32_e32 v19, 0x3fb8aa3b, v19
	v_sub_f32_e32 v20, v62, v60
	v_cndmask_b32_e32 v17, v17, v21, vcc
	v_exp_f32_e32 v19, v19
	v_mul_f32_e32 v20, 0x3fb8aa3b, v20
	v_sub_f32_e32 v21, v63, v60
	v_cmp_eq_u32_e32 vcc, 6, v39
	v_exp_f32_e32 v20, v20
	v_mul_f32_e32 v21, 0x3fb8aa3b, v21
	v_cndmask_b32_e32 v17, v17, v22, vcc
	v_cmp_eq_u32_e32 vcc, 7, v39
	v_exp_f32_e32 v21, v21
	v_add_f32_e32 v22, 0, v18
	v_cndmask_b32_e32 v17, v17, v23, vcc
	v_cmp_eq_u32_e32 vcc, 8, v39
	v_add_f32_e32 v22, v19, v22
	v_add_f32_e32 v22, v20, v22
	v_cndmask_b32_e32 v17, v17, v24, vcc
	v_cmp_eq_u32_e32 vcc, 9, v39
	v_sub_f32_e32 v23, v56, v60
	v_mul_f32_e32 v23, 0x3fb8aa3b, v23
	v_cndmask_b32_e32 v17, v17, v25, vcc
	v_cmp_eq_u32_e32 vcc, 10, v39
	v_sub_f32_e32 v24, v55, v60
	v_exp_f32_e32 v23, v23
	v_cndmask_b32_e32 v17, v17, v26, vcc
	v_add_f32_e32 v26, v21, v22
	v_sub_f32_e32 v22, v58, v60
	v_mul_f32_e32 v22, 0x3fb8aa3b, v22
	v_exp_f32_e32 v22, v22
	v_mul_f32_e32 v24, 0x3fb8aa3b, v24
	v_sub_f32_e32 v25, v54, v60
	v_exp_f32_e32 v24, v24
	v_mul_f32_e32 v25, 0x3fb8aa3b, v25
	v_cmp_eq_u32_e32 vcc, 11, v39
	v_exp_f32_e32 v25, v25
	v_add_f32_e32 v26, v22, v26
	v_cndmask_b32_e32 v17, v17, v27, vcc
	v_cmp_eq_u32_e32 vcc, 12, v39
	v_add_f32_e32 v26, v23, v26
	v_add_f32_e32 v26, v24, v26
	v_cndmask_b32_e32 v17, v17, v28, vcc
	v_cmp_eq_u32_e32 vcc, 13, v39
	v_sub_f32_e32 v27, v57, v60
	v_mul_f32_e32 v27, 0x3fb8aa3b, v27
	v_cndmask_b32_e32 v17, v17, v29, vcc
	v_cmp_eq_u32_e32 vcc, 14, v39
	v_sub_f32_e32 v28, v53, v60
	v_exp_f32_e32 v27, v27
	v_cndmask_b32_e32 v17, v17, v30, vcc
	v_add_f32_e32 v30, v25, v26
	v_sub_f32_e32 v26, v209, v60
	v_mul_f32_e32 v26, 0x3fb8aa3b, v26
	v_exp_f32_e32 v26, v26
	v_mul_f32_e32 v28, 0x3fb8aa3b, v28
	v_sub_f32_e32 v29, v52, v60
	v_exp_f32_e32 v28, v28
	v_mul_f32_e32 v29, 0x3fb8aa3b, v29
	v_exp_f32_e32 v29, v29
	v_exp_f32_e32 v34, v33
	v_sub_f32_e32 v33, v50, v60
	v_add_f32_e32 v30, v26, v30
	v_mul_f32_e32 v33, 0x3fb8aa3b, v33
	v_add_f32_e32 v30, v27, v30
	v_exp_f32_e32 v35, v33
	v_add_f32_e32 v30, v28, v30
	v_add_f32_e32 v30, v29, v30
	v_add_f32_e32 v12, v34, v30
	v_add_f32_e32 v12, v35, v12
	v_add_f32_e32 v12, v36, v12
	v_add_f32_e32 v30, v37, v12
	v_div_scale_f32 v32, s[6:7], v30, v30, 1.0
	v_rcp_f32_e32 v33, v32
	v_cmp_eq_u32_e32 vcc, 15, v39
	v_readlane_b32 s6, v255, 46
	s_lshl_b32 s6, s6, 4
	v_cndmask_b32_e32 v12, v17, v31, vcc
	v_fma_f32 v17, -v32, v33, 1.0
	v_fmac_f32_e32 v33, v17, v33
	v_div_scale_f32 v17, vcc, 1.0, v30, 1.0
	v_mul_f32_e32 v31, v17, v33
	v_lshl_add_u32 v12, v38, 7, v12
	v_fma_f32 v38, -v32, v31, v17
	v_fmac_f32_e32 v31, v38, v33
	v_fma_f32 v17, -v32, v31, v17
	v_div_fmas_f32 v17, v17, v33, v31
	v_div_fixup_f32 v30, v17, v30, 1.0
	v_lshlrev_b64 v[16:17], 9, v[176:177]
	s_ashr_i32 s7, s6, 31
	v_lshl_add_u64 v[32:33], s[94:95], 0, v[16:17]
	s_lshl_b64 s[6:7], s[6:7], 2
	v_lshl_add_u64 v[32:33], v[32:33], 0, s[6:7]
	v_lshl_add_u64 v[16:17], s[8:9], 0, v[16:17]
	v_lshl_add_u64 v[16:17], v[16:17], 0, s[6:7]
	global_store_dwordx4 v[32:33], v[12:15], off
	v_readlane_b32 s8, v255, 44
	v_readlane_b32 s9, v255, 45
	v_pk_mul_f32 v[12:13], v[18:19], v[30:31] op_sel_hi:[1,0]
	v_pk_mul_f32 v[14:15], v[20:21], v[30:31] op_sel_hi:[1,0]
	global_store_dwordx4 v[16:17], v[12:15], off
	global_store_dwordx4 v[32:33], v[8:11], off offset:16
	s_nop 1
	v_pk_mul_f32 v[8:9], v[22:23], v[30:31] op_sel_hi:[1,0]
	v_pk_mul_f32 v[10:11], v[24:25], v[30:31] op_sel_hi:[1,0]
	global_store_dwordx4 v[16:17], v[8:11], off offset:16
	global_store_dwordx4 v[32:33], v[4:7], off offset:32
	s_nop 1
	v_pk_mul_f32 v[4:5], v[26:27], v[30:31] op_sel_hi:[1,0]
	v_pk_mul_f32 v[6:7], v[28:29], v[30:31] op_sel_hi:[1,0]
	global_store_dwordx4 v[16:17], v[4:7], off offset:32
	global_store_dwordx4 v[32:33], v[0:3], off offset:48
	s_nop 1
	v_pk_mul_f32 v[0:1], v[34:35], v[30:31] op_sel_hi:[1,0]
	v_pk_mul_f32 v[2:3], v[36:37], v[30:31] op_sel_hi:[1,0]
	global_store_dwordx4 v[16:17], v[0:3], off offset:48
	s_branch .LBB0_696
